# attention: quarter-rate v_mul_lo_u32 by the constant row stride / LDS pitch replaced with full-rate shift-add pairs
# baseline (speedup 1.0000x reference)
; #define AT_LOADROWS(dst, l0, ls, col) do { _Pragma("unroll") for (int i_ = 0; i_ < 2; ++i_) { int l_ = (l0) + (ls) * (16 * i_ + lr); l_ = l_ < 0 ? 0 : (l_ > L - 1 ? L - 1 : l_); \
;         dst[i_] = *(const GAS u32x4*)(base + (size_t)l_ * rstride + (col)); } } while (0)
; #define AT_LDSWAIT() asm volatile("s_waitcnt lgkmcnt(0)" ::: "memory")
; #define AT_PUTRAW(src) do { _Pragma("unroll") for (int i_ = 0; i_ < 2; ++i_) *(LAS u32x4*)(stg + (16 * i_ + lr) * 80 + lc * 16) = src[i_]; } while (0)
; #define AT_GETRAW(dst) do { const i32x4 lo_ = *(const LAS i32x4*)(stg + r32 * 80 + 32 * hi), hi_ = *(const LAS i32x4*)(stg + r32 * 80 + 32 * hi + 16); dst = __builtin_shufflevector(lo_, hi_, 0, 1, 2, 3, 4, 5, 6, 7); } while (0)
; template <bool FIRST, int NB> ...
;     ...
;     const int r32 = lane & 31, hi = lane >> 5, lr = lane >> 2, lc = lane & 3;
;     const int qcol = ((g * 3 + 0) * 16 + h) * 64, kcol = ((g * 3 + 1) * 16 + h) * 64, vcol = ((g * 3 + 2) * 16 + h) * 64;
;     const size_t rstride = (size_t)dil * NQKV;
;     const unsigned char* base = QKVb + (size_t)cls * NQKV + lc * 16;
;     const int jlo = (kb0 >= -31) ? 0 : ((-kb0) >> 5);
;     const int qpos = q0 + QS * r32;
;     const int dmax = qpos < 128 ? qpos : 128;
;     const float half = 0.5f * (float)dmax;
;     ...
;     u32x4 kr[2][2];
;     i32x8 qf8;
;     { u32x4 qr[2]; AT_LOADROWS(qr, q0, QS, qcol);
; #pragma unroll
;       for (int j = 0; j < NB; ++j) if (j == jlo) AT_LOADROWS(kr[j & 1], kb0 + 32 * j, 1, kcol);
;       AT_PUTRAW(qr); AT_LDSWAIT(); AT_GETRAW(qf8); AT_LDSWAIT(); }
.LBB0_304:
	s_bfe_u32 s1, s0, 0x20001
	s_and_b32 s6, s0, 1
	s_and_b32 s2, s94, 1
	s_xor_b32 s3, s1, 3
	s_cmp_eq_u32 s2, 0
	s_cselect_b32 s38, s1, s3
	s_ashr_i32 s7, s0, 7
	s_bfe_u32 s39, s0, 0x40003
	s_lshl_b32 s8, s38, 9
	s_mul_i32 s1, s7, 0x1200000
	v_readlane_b32 s2, v253, 28
	s_mul_hi_i32 s0, s7, 0x1200000
	s_add_u32 s40, s2, s1
	v_readlane_b32 s1, v253, 29
	s_addc_u32 s41, s1, s0
	v_readlane_b32 s0, v255, 8
	v_mov_b32_e32 v114, v1
	s_add_i32 s10, s8, s0
	s_or_b32 s2, s10, s6
	s_waitcnt lgkmcnt(0)
	v_and_b32_e32 v126, 3, v114
	v_ashrrev_i32_e32 v125, 2, v114
	v_lshlrev_b32_e32 v2, 4, v126
	s_lshl_b32 s22, s39, 6
	v_lshl_add_u64 v[4:5], s[40:41], 0, v[2:3]
	v_lshl_add_u32 v6, v125, 1, s2
	v_lshl_add_u64 v[112:113], v[4:5], 0, s[22:23]
	v_min_i32_e32 v4, 0x7ff, v6
	v_cmp_lt_i32_e32 vcc, -1, v6
	v_add_u32_e32 v6, 32, v6
	v_lshl_add_u32 v4, v4, 3, v4
	v_lshlrev_b32_e32 v4, 10, v4
	v_min_i32_e32 v7, 0x7ff, v6
	v_cndmask_b32_e32 v4, 0, v4, vcc
	v_lshl_add_u32 v7, v7, 3, v7
	v_lshlrev_b32_e32 v7, 10, v7
	v_cmp_lt_i32_e32 vcc, -1, v6
	v_mov_b32_e32 v5, v3
	v_lshl_add_u64 v[4:5], v[112:113], 0, v[4:5]
	v_cndmask_b32_e32 v6, 0, v7, vcc
	v_mov_b32_e32 v7, v3
	v_lshl_add_u64 v[8:9], v[112:113], 0, v[6:7]
	global_load_dwordx4 v[4:7], v[4:5], off
	s_nop 0
	global_load_dwordx4 v[8:11], v[8:9], off
	s_sub_i32 s0, 0x80, s10
	s_add_i32 s3, s10, 0xffffff80
	s_ashr_i32 s0, s0, 5
	s_cmpk_lt_i32 s10, 0x61
	s_cselect_b32 s9, s0, 0
	s_cmp_eq_u32 s9, 0
	s_cselect_b64 s[46:47], -1, 0
	s_cmp_lg_u32 s9, 0
	v_add_u32_e32 v131, s3, v125
	s_cbranch_scc1 .LBB0_306
	v_min_i32_e32 v12, 0x7ff, v131
	v_add_u32_e32 v14, 16, v131
	v_lshl_add_u32 v12, v12, 3, v12
	v_lshlrev_b32_e32 v12, 10, v12
	v_cmp_lt_i32_e32 vcc, -1, v131
	v_min_i32_e32 v15, 0x7ff, v14
	v_mov_b32_e32 v13, v3
	v_cndmask_b32_e32 v12, 0, v12, vcc
	v_lshl_add_u32 v15, v15, 3, v15
	v_lshlrev_b32_e32 v15, 10, v15
	v_cmp_lt_i32_e32 vcc, -1, v14
	v_lshl_add_u64 v[12:13], v[112:113], 0, v[12:13]
	s_nop 0
	v_cndmask_b32_e32 v14, 0, v15, vcc
	v_mov_b32_e32 v15, v3
	v_lshl_add_u64 v[14:15], v[112:113], 0, v[14:15]
	global_load_dwordx4 v[68:71], v[12:13], off offset:1024
	global_load_dwordx4 v[72:75], v[14:15], off offset:1024
.LBB0_306:
	s_cmp_eq_u32 s9, 2
	v_add_u32_e32 v121, 64, v131
	v_add_u32_e32 v123, 0x50, v131
	s_mov_b32 s85, s51
	s_cselect_b64 s[48:49], -1, 0
	s_cmp_lg_u32 s9, 2
	v_min_i32_e32 v122, 0x7ff, v121
	v_cmp_lt_i32_e64 s[0:1], -1, v121
	v_min_i32_e32 v124, 0x7ff, v123
	v_cmp_lt_i32_e32 vcc, -1, v123
	s_cbranch_scc1 .LBB0_308
	v_lshl_add_u32 v12, v122, 3, v122
	v_lshlrev_b32_e32 v12, 10, v12
	v_cndmask_b32_e64 v12, 0, v12, s[0:1]
	v_mov_b32_e32 v13, v3
	v_lshl_add_u32 v14, v124, 3, v124
	v_lshlrev_b32_e32 v14, 10, v14
	v_lshl_add_u64 v[12:13], v[112:113], 0, v[12:13]
	v_cndmask_b32_e32 v14, 0, v14, vcc
	v_mov_b32_e32 v15, v3
	v_lshl_add_u64 v[14:15], v[112:113], 0, v[14:15]
	global_load_dwordx4 v[68:71], v[12:13], off offset:1024
	global_load_dwordx4 v[72:75], v[14:15], off offset:1024
.LBB0_308:
	s_cmp_eq_u32 s9, 4
	v_add_u32_e32 v117, s10, v125
	v_add_u32_e32 v119, 0x90, v131
	s_cselect_b64 s[50:51], -1, 0
	s_cmp_lg_u32 s9, 4
	v_min_i32_e32 v118, 0x7ff, v117
	v_cmp_lt_i32_e64 s[0:1], -1, v117
	v_min_i32_e32 v120, 0x7ff, v119
	v_cmp_lt_i32_e32 vcc, -1, v119
	s_cbranch_scc1 .LBB0_310
	v_lshl_add_u32 v12, v118, 3, v118
	v_lshlrev_b32_e32 v12, 10, v12
	v_cndmask_b32_e64 v12, 0, v12, s[0:1]
	v_mov_b32_e32 v13, v3
	v_lshl_add_u32 v14, v120, 3, v120
	v_lshlrev_b32_e32 v14, 10, v14
	v_lshl_add_u64 v[12:13], v[112:113], 0, v[12:13]
	v_cndmask_b32_e32 v14, 0, v14, vcc
	v_mov_b32_e32 v15, v3
	v_lshl_add_u64 v[14:15], v[112:113], 0, v[14:15]
	global_load_dwordx4 v[68:71], v[12:13], off offset:1024
	global_load_dwordx4 v[72:75], v[14:15], off offset:1024
; template <bool FIRST, int NB> ...
;     ...
;     const int r32 = lane & 31, hi = lane >> 5, lr = lane >> 2, lc = lane & 3;
;     const int qcol = ((g * 3 + 0) * 16 + h) * 64, kcol = ((g * 3 + 1) * 16 + h) * 64, vcol = ((g * 3 + 2) * 16 + h) * 64;
;     const size_t rstride = (size_t)dil * NQKV;
;     const unsigned char* base = QKVb + (size_t)cls * NQKV + lc * 16;
;     const int jlo = (kb0 >= -31) ? 0 : ((-kb0) >> 5);
;     const int qpos = q0 + QS * r32;
;     const int dmax = qpos < 128 ? qpos : 128;
;     const float half = 0.5f * (float)dmax;
;     ...
;     u32x4 kr[2][2];
;     i32x8 qf8;
;     { u32x4 qr[2]; AT_LOADROWS(qr, q0, QS, qcol);
; #pragma unroll
;       for (int j = 0; j < NB; ++j) if (j == jlo) AT_LOADROWS(kr[j & 1], kb0 + 32 * j, 1, kcol);
;       AT_PUTRAW(qr); AT_LDSWAIT(); AT_GETRAW(qf8); AT_LDSWAIT(); }
;     f32x16 S[NB];
;     float mx = -INFINITY;
; #pragma unroll
;     for (int j = 0; j < NB; ++j) {
;         if (j >= jlo) {
;             asm volatile("" ::: "memory");
;             if (j < NB - 1) AT_LOADROWS(kr[(j + 1) & 1], kb0 + 32 * (j + 1), 1, kcol);
;             AT_PUTRAW(kr[j & 1]);
;             const float xd0 = (float)(qpos - kb0 - 32 * j - 4 * hi) - half;
;             const bool inner = (q0 - kb0 - 32 * j - 31 >= 0) && (q0 + QS * 31 - kb0 - 32 * j <= 128) && (kb0 + 32 * j >= 0);
;             f32x16 a;
;             if (inner) {
;                 const float cb = -slope2d * xd0;
; #pragma unroll
;                 for (int r = 0; r < 16; ++r) a[r] = __builtin_fmaf(slope2d, (float)((r & 3) + 8 * (r >> 2)), cb);
;             } else {
;                 const f32x2 xd2 = {xd0, xd0}, ns2 = {-slope2d, -slope2d};
; #pragma unroll
;                 for (int r = 0; r < 16; r += 2) { const f32x2 c2 = {(float)((r & 3) + 8 * (r >> 2)), (float)(((r + 1) & 3) + 8 * ((r + 1) >> 2))};
;                     const f32x2 x2 = xd2 - c2, b2 = x2 * ns2;
;                     a[r] = (__builtin_fabsf(x2[0]) <= half) ? b2[0] : -INFINITY; a[r + 1] = (__builtin_fabsf(x2[1]) <= half) ? b2[1] : -INFINITY; }
;             }
;             i32x8 kf8;
;             AT_LDSWAIT(); AT_GETRAW(kf8); AT_LDSWAIT();
;             a = __builtin_amdgcn_mfma_scale_f32_32x32x64_f8f6f4(kf8, qf8, a, 0, 0, 0, 0x797b, 1, 0x797b);
; #pragma unroll
;             for (int r = 0; r < 16; ++r) mx = fmaxf(mx, a[r]);
;             S[j] = a;
.LBB0_310:
	s_not_b32 s0, s39
	s_lshl_b32 s0, s0, 3
	v_cvt_f32_i32_e32 v12, s0
	s_mov_b32 s11, 0x42400000
	v_add_u32_e32 v2, s77, v2
	v_and_b32_e32 v111, 31, v114
	v_div_scale_f32 v13, s[0:1], s11, s11, v12
	v_rcp_f32_e32 v14, v13
	v_div_scale_f32 v15, vcc, v12, s11, v12
	s_mov_b32 s0, 0xc2fc0000
	v_fma_f32 v16, -v13, v14, 1.0
	v_fmac_f32_e32 v14, v16, v14
	v_mul_f32_e32 v16, v15, v14
	v_fma_f32 v17, -v13, v16, v15
	v_fmac_f32_e32 v16, v17, v14
	v_fma_f32 v13, -v13, v16, v15
	v_div_fmas_f32 v13, v13, v14, v16
	v_div_fixup_f32 v12, v13, s11, v12
	v_cmp_gt_f32_e32 vcc, s0, v12
	s_and_b64 s[0:1], vcc, exec
	s_cselect_b32 s0, 0xffffffc0, 0
	v_cndmask_b32_e32 v13, 0, v226, vcc
	v_add_f32_e32 v12, v12, v13
	v_exp_f32_e32 v12, v12
	v_lshl_or_b32 v13, v111, 1, s2
	s_or_b32 s11, s2, 62
	s_cmp_lt_i32 s9, 1
	v_ldexp_f32 v12, v12, s0
	s_movk_i32 s0, 0x50
	v_mul_lo_u32 v14, v125, s0
	v_add_u32_e32 v85, v2, v14
	v_mov_b32_e32 v2, s77
	s_waitcnt vmcnt(0)
	ds_write_b128 v85, v[4:7]
	ds_write_b128 v85, v[8:11] offset:1280
	v_mad_u32_u24 v2, v111, s0, v2
	v_and_b32_e32 v4, 0xffffffe0, v114
	v_mul_f32_e32 v110, 0x3fb8aa3b, v12
	v_min_i32_e32 v12, 0x80, v13
	s_waitcnt lgkmcnt(0)
	v_add_u32_e32 v145, v2, v4
	v_cvt_f32_i32_e32 v12, v12
	ds_read_b128 v[100:103], v145
	ds_read_b128 v[104:107], v145 offset:16
	v_ashrrev_i32_e32 v2, 3, v114
	s_waitcnt lgkmcnt(0)
	v_and_b32_e32 v116, -4, v2
	v_xor_b32_e32 v98, 0x80000000, v110
	v_add_u32_e32 v127, 32, v131
	v_add_u32_e32 v129, 48, v131
	v_add_u32_e32 v2, s10, v116
	v_mul_f32_e32 v115, 0.5, v12
	v_mov_b32_e32 v99, v98
	v_mov_b32_e32 v19, 0xff800000
	s_cselect_b64 s[42:43], -1, 0
	s_cmp_gt_i32 s9, 0
	v_min_i32_e32 v128, 0x7ff, v127
	v_cmp_lt_i32_e64 s[0:1], -1, v127
	v_min_i32_e32 v130, 0x7ff, v129
	v_cmp_lt_i32_e32 vcc, -1, v129
	v_sub_u32_e32 v94, v13, v2
	v_mov_b32_e32 v18, 0xff800000
	v_mov_b32_e32 v17, 0xff800000
	v_mov_b32_e32 v16, 0xff800000
	v_mov_b32_e32 v15, 0xff800000
	v_mov_b32_e32 v14, 0xff800000
	v_mov_b32_e32 v13, 0xff800000
	v_mov_b32_e32 v12, 0xff800000
	v_mov_b32_e32 v11, 0xff800000
	v_mov_b32_e32 v10, 0xff800000
	v_mov_b32_e32 v9, 0xff800000
	v_mov_b32_e32 v8, 0xff800000
	v_mov_b32_e32 v7, 0xff800000
	v_mov_b32_e32 v6, 0xff800000
	v_mov_b32_e32 v5, 0xff800000
	v_mov_b32_e32 v4, 0xff800000
	v_mov_b32_e32 v150, 0xff800000
	s_cbranch_scc1 .LBB0_316
	v_lshl_add_u32 v2, v128, 3, v128
	v_lshlrev_b32_e32 v2, 10, v2
	v_cndmask_b32_e64 v2, 0, v2, s[0:1]
	v_lshl_add_u64 v[4:5], v[112:113], 0, v[2:3]
	v_lshl_add_u32 v2, v130, 3, v130
	v_lshlrev_b32_e32 v2, 10, v2
	v_cndmask_b32_e32 v2, 0, v2, vcc
	v_lshl_add_u64 v[6:7], v[112:113], 0, v[2:3]
	global_load_dwordx4 v[86:89], v[4:5], off offset:1024
	global_load_dwordx4 v[90:93], v[6:7], off offset:1024
	v_add_u32_e32 v2, 0x80, v94
	s_sub_i32 s0, s11, s3
	v_cvt_f32_i32_e32 v2, v2
	s_cmpk_gt_i32 s0, 0x80
	s_cselect_b64 s[0:1], -1, 0
	s_cmpk_lt_i32 s10, 0x80
	s_cselect_b64 s[44:45], -1, 0
	s_or_b64 s[44:45], s[44:45], s[0:1]
	v_sub_f32_e32 v2, v2, v115
	s_mov_b64 s[0:1], -1
	s_and_b64 vcc, exec, s[44:45]
	ds_write_b128 v85, v[68:71]
	ds_write_b128 v85, v[72:75] offset:1280
	s_cbranch_vccz .LBB0_313
	s_brev_b32 s0, 1
	s_mov_b32 s1, -1.0
	v_pk_add_f32 v[4:5], v[2:3], s[0:1] op_sel_hi:[0,1]
	v_pk_mul_f32 v[6:7], v[98:99], v[4:5]
	v_cmp_le_f32_e64 vcc, |v4|, v115
	s_mov_b32 s0, -2.0
	s_mov_b32 s1, 0xc0400000
	v_cndmask_b32_e32 v4, v227, v6, vcc
	v_cmp_le_f32_e64 vcc, |v5|, v115
	s_nop 1
	v_cndmask_b32_e32 v5, v227, v7, vcc
	v_pk_add_f32 v[6:7], v[2:3], s[0:1] op_sel_hi:[0,1]
	v_pk_mul_f32 v[8:9], v[98:99], v[6:7]
	v_cmp_le_f32_e64 vcc, |v6|, v115
	s_mov_b32 s0, 0xc1000000
	s_mov_b32 s1, 0xc1100000
	v_cndmask_b32_e32 v6, v227, v8, vcc
	v_cmp_le_f32_e64 vcc, |v7|, v115
	s_nop 1
	v_cndmask_b32_e32 v7, v227, v9, vcc
	v_pk_add_f32 v[8:9], v[2:3], s[0:1] op_sel_hi:[0,1]
	v_pk_mul_f32 v[10:11], v[98:99], v[8:9]
	v_cmp_le_f32_e64 vcc, |v8|, v115
	s_mov_b32 s0, 0xc1200000
	s_mov_b32 s1, 0xc1300000
	v_cndmask_b32_e32 v8, v227, v10, vcc
	v_cmp_le_f32_e64 vcc, |v9|, v115
	s_nop 1
	v_cndmask_b32_e32 v9, v227, v11, vcc
	v_pk_add_f32 v[10:11], v[2:3], s[0:1] op_sel_hi:[0,1]
	v_pk_mul_f32 v[12:13], v[98:99], v[10:11]
	v_cmp_le_f32_e64 vcc, |v10|, v115
	s_mov_b32 s0, 0xc1800000
	s_mov_b32 s1, 0xc1880000
	v_cndmask_b32_e32 v10, v227, v12, vcc
	v_cmp_le_f32_e64 vcc, |v11|, v115
	s_nop 1
	v_cndmask_b32_e32 v11, v227, v13, vcc
	v_pk_add_f32 v[12:13], v[2:3], s[0:1] op_sel_hi:[0,1]
	v_pk_mul_f32 v[14:15], v[98:99], v[12:13]
	v_cmp_le_f32_e64 vcc, |v12|, v115
	s_mov_b32 s0, 0xc1900000
	s_mov_b32 s1, 0xc1980000
	v_cndmask_b32_e32 v12, v227, v14, vcc
	v_cmp_le_f32_e64 vcc, |v13|, v115
	s_nop 1
	v_cndmask_b32_e32 v13, v227, v15, vcc
	v_pk_add_f32 v[14:15], v[2:3], s[0:1] op_sel_hi:[0,1]
	v_pk_mul_f32 v[16:17], v[98:99], v[14:15]
	v_cmp_le_f32_e64 vcc, |v14|, v115
	s_mov_b32 s0, 0xc1c00000
	s_mov_b32 s1, 0xc1c80000
	v_cndmask_b32_e32 v14, v227, v16, vcc
	v_cmp_le_f32_e64 vcc, |v15|, v115
	s_nop 1
	v_cndmask_b32_e32 v15, v227, v17, vcc
	v_pk_add_f32 v[16:17], v[2:3], s[0:1] op_sel_hi:[0,1]
	v_pk_mul_f32 v[18:19], v[98:99], v[16:17]
	v_cmp_le_f32_e64 vcc, |v16|, v115
	s_mov_b32 s0, 0xc1d00000
	s_mov_b32 s1, 0xc1d80000
	v_cndmask_b32_e32 v16, v227, v18, vcc
	v_cmp_le_f32_e64 vcc, |v17|, v115
	s_nop 1
	v_cndmask_b32_e32 v17, v227, v19, vcc
	v_pk_add_f32 v[18:19], v[2:3], s[0:1] op_sel_hi:[0,1]
	v_pk_mul_f32 v[20:21], v[98:99], v[18:19]
	v_cmp_le_f32_e64 vcc, |v18|, v115
	s_mov_b64 s[0:1], 0
	s_nop 0
	v_cndmask_b32_e32 v18, v227, v20, vcc
	v_cmp_le_f32_e64 vcc, |v19|, v115
	s_nop 1
	v_cndmask_b32_e32 v19, v227, v21, vcc

; #define AT_LOADROWS(dst, l0, ls, col) do { _Pragma("unroll") for (int i_ = 0; i_ < 2; ++i_) { int l_ = (l0) + (ls) * (16 * i_ + lr); l_ = l_ < 0 ? 0 : (l_ > L - 1 ? L - 1 : l_); \
;         dst[i_] = *(const GAS u32x4*)(base + (size_t)l_ * rstride + (col)); } } while (0)
; #define AT_LDSWAIT() asm volatile("s_waitcnt lgkmcnt(0)" ::: "memory")
; #define AT_PUTRAW(src) do { _Pragma("unroll") for (int i_ = 0; i_ < 2; ++i_) *(LAS u32x4*)(stg + (16 * i_ + lr) * 80 + lc * 16) = src[i_]; } while (0)
; #define AT_GETRAW(dst) do { const i32x4 lo_ = *(const LAS i32x4*)(stg + r32 * 80 + 32 * hi), hi_ = *(const LAS i32x4*)(stg + r32 * 80 + 32 * hi + 16); dst = __builtin_shufflevector(lo_, hi_, 0, 1, 2, 3, 4, 5, 6, 7); } while (0)
; template <bool FIRST, int NB> ...
;     ...
;     for (int j = 0; j < NB; ++j) {
;         if (j >= jlo) {
;             asm volatile("" ::: "memory");
;             if (j < NB - 1) AT_LOADROWS(kr[(j + 1) & 1], kb0 + 32 * (j + 1), 1, kcol);
;             AT_PUTRAW(kr[j & 1]);
;             const float xd0 = (float)(qpos - kb0 - 32 * j - 4 * hi) - half;
;             const bool inner = (q0 - kb0 - 32 * j - 31 >= 0) && (q0 + QS * 31 - kb0 - 32 * j <= 128) && (kb0 + 32 * j >= 0);
;             f32x16 a;
;             if (inner) {
;                 const float cb = -slope2d * xd0;
; #pragma unroll
;                 for (int r = 0; r < 16; ++r) a[r] = __builtin_fmaf(slope2d, (float)((r & 3) + 8 * (r >> 2)), cb);
;             } else {
;                 const f32x2 xd2 = {xd0, xd0}, ns2 = {-slope2d, -slope2d};
; #pragma unroll
;                 for (int r = 0; r < 16; r += 2) { const f32x2 c2 = {(float)((r & 3) + 8 * (r >> 2)), (float)(((r + 1) & 3) + 8 * ((r + 1) >> 2))};
;                     const f32x2 x2 = xd2 - c2, b2 = x2 * ns2;
;                     a[r] = (__builtin_fabsf(x2[0]) <= half) ? b2[0] : -INFINITY; a[r + 1] = (__builtin_fabsf(x2[1]) <= half) ? b2[1] : -INFINITY; }
;             }
;             i32x8 kf8;
;             AT_LDSWAIT(); AT_GETRAW(kf8); AT_LDSWAIT();
;             a = __builtin_amdgcn_mfma_scale_f32_32x32x64_f8f6f4(kf8, qf8, a, 0, 0, 0, 0x797b, 1, 0x797b);
; #pragma unroll
;             for (int r = 0; r < 16; ++r) mx = fmaxf(mx, a[r]);
;             S[j] = a;
.LBB0_316:
	s_cmp_lt_i32 s9, 2
	s_cselect_b64 s[44:45], -1, 0
	s_cmp_gt_i32 s9, 1
	v_mov_b32_e32 v35, 0xff800000
	s_cbranch_scc1 .LBB0_322
	v_lshl_add_u32 v2, v122, 3, v122
	v_lshlrev_b32_e32 v2, 10, v2
	v_cmp_lt_i32_e32 vcc, -1, v121
	s_sub_i32 s0, s11, s10
	s_addk_i32 s0, 0x60
	v_cndmask_b32_e32 v2, 0, v2, vcc
	v_lshl_add_u64 v[20:21], v[112:113], 0, v[2:3]
	v_lshl_add_u32 v2, v124, 3, v124
	v_lshlrev_b32_e32 v2, 10, v2
	v_cmp_lt_i32_e32 vcc, -1, v123
	s_cmpk_lt_i32 s0, 0x81
	s_cselect_b64 s[0:1], -1, 0
	v_cndmask_b32_e32 v2, 0, v2, vcc
	v_lshl_add_u64 v[22:23], v[112:113], 0, v[2:3]
	global_load_dwordx4 v[68:71], v[20:21], off offset:1024
	global_load_dwordx4 v[72:75], v[22:23], off offset:1024
	v_add_u32_e32 v2, 0x60, v94
	v_cvt_f32_i32_e32 v2, v2
	s_cmpk_gt_i32 s10, 0x5f
	s_cselect_b64 s[52:53], -1, 0
	s_and_b64 s[52:53], s[52:53], s[0:1]
	v_sub_f32_e32 v2, v2, v115
	s_mov_b64 s[0:1], -1
	s_and_b64 vcc, exec, s[52:53]
	s_waitcnt vmcnt(3)
	ds_write_b128 v85, v[86:89]
	s_waitcnt vmcnt(2)
	ds_write_b128 v85, v[90:93] offset:1280
	s_cbranch_vccnz .LBB0_319
	s_brev_b32 s0, 1
	s_mov_b32 s1, -1.0
	v_pk_add_f32 v[20:21], v[2:3], s[0:1] op_sel_hi:[0,1]
	v_pk_mul_f32 v[22:23], v[98:99], v[20:21]
	v_cmp_le_f32_e64 vcc, |v20|, v115
	s_mov_b32 s0, -2.0
	s_mov_b32 s1, 0xc0400000
	v_cndmask_b32_e32 v20, v227, v22, vcc
	v_cmp_le_f32_e64 vcc, |v21|, v115
	s_nop 1
	v_cndmask_b32_e32 v21, v227, v23, vcc
	v_pk_add_f32 v[22:23], v[2:3], s[0:1] op_sel_hi:[0,1]
	v_pk_mul_f32 v[24:25], v[98:99], v[22:23]
	v_cmp_le_f32_e64 vcc, |v22|, v115
	s_mov_b32 s0, 0xc1000000
	s_mov_b32 s1, 0xc1100000
	v_cndmask_b32_e32 v22, v227, v24, vcc
	v_cmp_le_f32_e64 vcc, |v23|, v115
	s_nop 1
	v_cndmask_b32_e32 v23, v227, v25, vcc
	v_pk_add_f32 v[24:25], v[2:3], s[0:1] op_sel_hi:[0,1]
	v_pk_mul_f32 v[26:27], v[98:99], v[24:25]
	v_cmp_le_f32_e64 vcc, |v24|, v115
	s_mov_b32 s0, 0xc1200000
	s_mov_b32 s1, 0xc1300000
	v_cndmask_b32_e32 v24, v227, v26, vcc
	v_cmp_le_f32_e64 vcc, |v25|, v115
	s_nop 1
	v_cndmask_b32_e32 v25, v227, v27, vcc
	v_pk_add_f32 v[26:27], v[2:3], s[0:1] op_sel_hi:[0,1]
	v_pk_mul_f32 v[28:29], v[98:99], v[26:27]
	v_cmp_le_f32_e64 vcc, |v26|, v115
	s_mov_b32 s0, 0xc1800000
	s_mov_b32 s1, 0xc1880000
	v_cndmask_b32_e32 v26, v227, v28, vcc
	v_cmp_le_f32_e64 vcc, |v27|, v115
	s_nop 1
	v_cndmask_b32_e32 v27, v227, v29, vcc
	v_pk_add_f32 v[28:29], v[2:3], s[0:1] op_sel_hi:[0,1]
	v_pk_mul_f32 v[30:31], v[98:99], v[28:29]
	v_cmp_le_f32_e64 vcc, |v28|, v115
	s_mov_b32 s0, 0xc1900000
	s_mov_b32 s1, 0xc1980000
	v_cndmask_b32_e32 v28, v227, v30, vcc
	v_cmp_le_f32_e64 vcc, |v29|, v115
	s_nop 1
	v_cndmask_b32_e32 v29, v227, v31, vcc
	v_pk_add_f32 v[30:31], v[2:3], s[0:1] op_sel_hi:[0,1]
	v_pk_mul_f32 v[32:33], v[98:99], v[30:31]
	v_cmp_le_f32_e64 vcc, |v30|, v115
	s_mov_b32 s0, 0xc1c00000
	s_mov_b32 s1, 0xc1c80000
	v_cndmask_b32_e32 v30, v227, v32, vcc
	v_cmp_le_f32_e64 vcc, |v31|, v115
	s_nop 1
	v_cndmask_b32_e32 v31, v227, v33, vcc
	v_pk_add_f32 v[32:33], v[2:3], s[0:1] op_sel_hi:[0,1]
	v_pk_mul_f32 v[34:35], v[98:99], v[32:33]
	v_cmp_le_f32_e64 vcc, |v32|, v115
	s_mov_b32 s0, 0xc1d00000
	s_mov_b32 s1, 0xc1d80000
	v_cndmask_b32_e32 v32, v227, v34, vcc
	v_cmp_le_f32_e64 vcc, |v33|, v115
	s_nop 1
	v_cndmask_b32_e32 v33, v227, v35, vcc
	v_pk_add_f32 v[34:35], v[2:3], s[0:1] op_sel_hi:[0,1]
	v_pk_mul_f32 v[36:37], v[98:99], v[34:35]
	v_cmp_le_f32_e64 vcc, |v34|, v115
	s_mov_b64 s[0:1], 0
	s_nop 0
	v_cndmask_b32_e32 v34, v227, v36, vcc
	v_cmp_le_f32_e64 vcc, |v35|, v115
	s_nop 1
	v_cndmask_b32_e32 v35, v227, v37, vcc

; #define AT_LOADROWS(dst, l0, ls, col) do { _Pragma("unroll") for (int i_ = 0; i_ < 2; ++i_) { int l_ = (l0) + (ls) * (16 * i_ + lr); l_ = l_ < 0 ? 0 : (l_ > L - 1 ? L - 1 : l_); \
;         dst[i_] = *(const GAS u32x4*)(base + (size_t)l_ * rstride + (col)); } } while (0)
; #define AT_LDSWAIT() asm volatile("s_waitcnt lgkmcnt(0)" ::: "memory")
; #define AT_PUTRAW(src) do { _Pragma("unroll") for (int i_ = 0; i_ < 2; ++i_) *(LAS u32x4*)(stg + (16 * i_ + lr) * 80 + lc * 16) = src[i_]; } while (0)
; #define AT_GETRAW(dst) do { const i32x4 lo_ = *(const LAS i32x4*)(stg + r32 * 80 + 32 * hi), hi_ = *(const LAS i32x4*)(stg + r32 * 80 + 32 * hi + 16); dst = __builtin_shufflevector(lo_, hi_, 0, 1, 2, 3, 4, 5, 6, 7); } while (0)
; template <bool FIRST, int NB> ...
;     ...
;     for (int j = 0; j < NB; ++j) {
;         if (j >= jlo) {
;             asm volatile("" ::: "memory");
;             if (j < NB - 1) AT_LOADROWS(kr[(j + 1) & 1], kb0 + 32 * (j + 1), 1, kcol);
;             AT_PUTRAW(kr[j & 1]);
;             const float xd0 = (float)(qpos - kb0 - 32 * j - 4 * hi) - half;
;             const bool inner = (q0 - kb0 - 32 * j - 31 >= 0) && (q0 + QS * 31 - kb0 - 32 * j <= 128) && (kb0 + 32 * j >= 0);
;             f32x16 a;
;             if (inner) {
;                 const float cb = -slope2d * xd0;
; #pragma unroll
;                 for (int r = 0; r < 16; ++r) a[r] = __builtin_fmaf(slope2d, (float)((r & 3) + 8 * (r >> 2)), cb);
;             } else {
;                 const f32x2 xd2 = {xd0, xd0}, ns2 = {-slope2d, -slope2d};
; #pragma unroll
;                 for (int r = 0; r < 16; r += 2) { const f32x2 c2 = {(float)((r & 3) + 8 * (r >> 2)), (float)(((r + 1) & 3) + 8 * ((r + 1) >> 2))};
;                     const f32x2 x2 = xd2 - c2, b2 = x2 * ns2;
;                     a[r] = (__builtin_fabsf(x2[0]) <= half) ? b2[0] : -INFINITY; a[r + 1] = (__builtin_fabsf(x2[1]) <= half) ? b2[1] : -INFINITY; }
;             }
;             i32x8 kf8;
;             AT_LDSWAIT(); AT_GETRAW(kf8); AT_LDSWAIT();
;             a = __builtin_amdgcn_mfma_scale_f32_32x32x64_f8f6f4(kf8, qf8, a, 0, 0, 0, 0x797b, 1, 0x797b);
; #pragma unroll
;             for (int r = 0; r < 16; ++r) mx = fmaxf(mx, a[r]);
;             S[j] = a;
.LBB0_323:
	s_cmp_lt_i32 s9, 3
	v_add_u32_e32 v132, 0x60, v131
	v_add_u32_e32 v143, 0x70, v131
	v_mov_b32_e32 v51, 0xff800000
	s_cselect_b64 s[52:53], -1, 0
	s_cmp_gt_i32 s9, 2
	v_min_i32_e32 v133, 0x7ff, v132
	v_cmp_lt_i32_e64 s[0:1], -1, v132
	v_min_i32_e32 v144, 0x7ff, v143
	v_cmp_lt_i32_e32 vcc, -1, v143
	s_cbranch_scc1 .LBB0_329
	v_lshl_add_u32 v2, v133, 3, v133
	v_lshlrev_b32_e32 v2, 10, v2
	v_cndmask_b32_e64 v2, 0, v2, s[0:1]
	v_lshl_add_u64 v[36:37], v[112:113], 0, v[2:3]
	v_lshl_add_u32 v2, v144, 3, v144
	v_lshlrev_b32_e32 v2, 10, v2
	v_cndmask_b32_e32 v2, 0, v2, vcc
	v_lshl_add_u64 v[38:39], v[112:113], 0, v[2:3]
	global_load_dwordx4 v[86:89], v[36:37], off offset:1024
	global_load_dwordx4 v[90:93], v[38:39], off offset:1024
	s_sub_i32 s0, s11, s10
	v_add_u32_e32 v2, 64, v94
	s_add_i32 s0, s0, 64
	v_cvt_f32_i32_e32 v2, v2
	s_cmpk_lt_i32 s0, 0x81
	s_cselect_b64 s[0:1], -1, 0
	s_cmp_gt_i32 s10, 63
	s_cselect_b64 s[54:55], -1, 0
	s_and_b64 s[54:55], s[54:55], s[0:1]
	v_sub_f32_e32 v2, v2, v115
	s_mov_b64 s[0:1], -1
	s_and_b64 vcc, exec, s[54:55]
	s_waitcnt vmcnt(3)
	ds_write_b128 v85, v[68:71]
	s_waitcnt vmcnt(2)
	ds_write_b128 v85, v[72:75] offset:1280
	s_cbranch_vccnz .LBB0_326
	s_brev_b32 s0, 1
	s_mov_b32 s1, -1.0
	v_pk_add_f32 v[36:37], v[2:3], s[0:1] op_sel_hi:[0,1]
	v_pk_mul_f32 v[38:39], v[98:99], v[36:37]
	v_cmp_le_f32_e64 vcc, |v36|, v115
	s_mov_b32 s0, -2.0
	s_mov_b32 s1, 0xc0400000
	v_cndmask_b32_e32 v36, v227, v38, vcc
	v_cmp_le_f32_e64 vcc, |v37|, v115
	s_nop 1
	v_cndmask_b32_e32 v37, v227, v39, vcc
	v_pk_add_f32 v[38:39], v[2:3], s[0:1] op_sel_hi:[0,1]
	v_pk_mul_f32 v[40:41], v[98:99], v[38:39]
	v_cmp_le_f32_e64 vcc, |v38|, v115
	s_mov_b32 s0, 0xc1000000
	s_mov_b32 s1, 0xc1100000
	v_cndmask_b32_e32 v38, v227, v40, vcc
	v_cmp_le_f32_e64 vcc, |v39|, v115
	s_nop 1
	v_cndmask_b32_e32 v39, v227, v41, vcc
	v_pk_add_f32 v[40:41], v[2:3], s[0:1] op_sel_hi:[0,1]
	v_pk_mul_f32 v[42:43], v[98:99], v[40:41]
	v_cmp_le_f32_e64 vcc, |v40|, v115
	s_mov_b32 s0, 0xc1200000
	s_mov_b32 s1, 0xc1300000
	v_cndmask_b32_e32 v40, v227, v42, vcc
	v_cmp_le_f32_e64 vcc, |v41|, v115
	s_nop 1
	v_cndmask_b32_e32 v41, v227, v43, vcc
	v_pk_add_f32 v[42:43], v[2:3], s[0:1] op_sel_hi:[0,1]
	v_pk_mul_f32 v[44:45], v[98:99], v[42:43]
	v_cmp_le_f32_e64 vcc, |v42|, v115
	s_mov_b32 s0, 0xc1800000
	s_mov_b32 s1, 0xc1880000
	v_cndmask_b32_e32 v42, v227, v44, vcc
	v_cmp_le_f32_e64 vcc, |v43|, v115
	s_nop 1
	v_cndmask_b32_e32 v43, v227, v45, vcc
	v_pk_add_f32 v[44:45], v[2:3], s[0:1] op_sel_hi:[0,1]
	v_pk_mul_f32 v[46:47], v[98:99], v[44:45]
	v_cmp_le_f32_e64 vcc, |v44|, v115
	s_mov_b32 s0, 0xc1900000
	s_mov_b32 s1, 0xc1980000
	v_cndmask_b32_e32 v44, v227, v46, vcc
	v_cmp_le_f32_e64 vcc, |v45|, v115
	s_nop 1
	v_cndmask_b32_e32 v45, v227, v47, vcc
	v_pk_add_f32 v[46:47], v[2:3], s[0:1] op_sel_hi:[0,1]
	v_pk_mul_f32 v[48:49], v[98:99], v[46:47]
	v_cmp_le_f32_e64 vcc, |v46|, v115
	s_mov_b32 s0, 0xc1c00000
	s_mov_b32 s1, 0xc1c80000
	v_cndmask_b32_e32 v46, v227, v48, vcc
	v_cmp_le_f32_e64 vcc, |v47|, v115
	s_nop 1
	v_cndmask_b32_e32 v47, v227, v49, vcc
	v_pk_add_f32 v[48:49], v[2:3], s[0:1] op_sel_hi:[0,1]
	v_pk_mul_f32 v[50:51], v[98:99], v[48:49]
	v_cmp_le_f32_e64 vcc, |v48|, v115
	s_mov_b32 s0, 0xc1d00000
	s_mov_b32 s1, 0xc1d80000
	v_cndmask_b32_e32 v48, v227, v50, vcc
	v_cmp_le_f32_e64 vcc, |v49|, v115
	s_nop 1
	v_cndmask_b32_e32 v49, v227, v51, vcc
	v_pk_add_f32 v[50:51], v[2:3], s[0:1] op_sel_hi:[0,1]
	v_pk_mul_f32 v[52:53], v[98:99], v[50:51]
	v_cmp_le_f32_e64 vcc, |v50|, v115
	s_mov_b64 s[0:1], 0
	s_nop 0
	v_cndmask_b32_e32 v50, v227, v52, vcc
	v_cmp_le_f32_e64 vcc, |v51|, v115
	s_nop 1
	v_cndmask_b32_e32 v51, v227, v53, vcc

; #define AT_LOADROWS(dst, l0, ls, col) do { _Pragma("unroll") for (int i_ = 0; i_ < 2; ++i_) { int l_ = (l0) + (ls) * (16 * i_ + lr); l_ = l_ < 0 ? 0 : (l_ > L - 1 ? L - 1 : l_); \
;         dst[i_] = *(const GAS u32x4*)(base + (size_t)l_ * rstride + (col)); } } while (0)
; #define AT_LDSWAIT() asm volatile("s_waitcnt lgkmcnt(0)" ::: "memory")
; #define AT_PUTRAW(src) do { _Pragma("unroll") for (int i_ = 0; i_ < 2; ++i_) *(LAS u32x4*)(stg + (16 * i_ + lr) * 80 + lc * 16) = src[i_]; } while (0)
; #define AT_GETRAW(dst) do { const i32x4 lo_ = *(const LAS i32x4*)(stg + r32 * 80 + 32 * hi), hi_ = *(const LAS i32x4*)(stg + r32 * 80 + 32 * hi + 16); dst = __builtin_shufflevector(lo_, hi_, 0, 1, 2, 3, 4, 5, 6, 7); } while (0)
; template <bool FIRST, int NB> ...
;     ...
;     for (int j = 0; j < NB; ++j) {
;         if (j >= jlo) {
;             asm volatile("" ::: "memory");
;             if (j < NB - 1) AT_LOADROWS(kr[(j + 1) & 1], kb0 + 32 * (j + 1), 1, kcol);
;             AT_PUTRAW(kr[j & 1]);
;             const float xd0 = (float)(qpos - kb0 - 32 * j - 4 * hi) - half;
;             const bool inner = (q0 - kb0 - 32 * j - 31 >= 0) && (q0 + QS * 31 - kb0 - 32 * j <= 128) && (kb0 + 32 * j >= 0);
;             f32x16 a;
;             if (inner) {
;                 const float cb = -slope2d * xd0;
; #pragma unroll
;                 for (int r = 0; r < 16; ++r) a[r] = __builtin_fmaf(slope2d, (float)((r & 3) + 8 * (r >> 2)), cb);
;             } else {
;                 const f32x2 xd2 = {xd0, xd0}, ns2 = {-slope2d, -slope2d};
; #pragma unroll
;                 for (int r = 0; r < 16; r += 2) { const f32x2 c2 = {(float)((r & 3) + 8 * (r >> 2)), (float)(((r + 1) & 3) + 8 * ((r + 1) >> 2))};
;                     const f32x2 x2 = xd2 - c2, b2 = x2 * ns2;
;                     a[r] = (__builtin_fabsf(x2[0]) <= half) ? b2[0] : -INFINITY; a[r + 1] = (__builtin_fabsf(x2[1]) <= half) ? b2[1] : -INFINITY; }
;             }
;             i32x8 kf8;
;             AT_LDSWAIT(); AT_GETRAW(kf8); AT_LDSWAIT();
;             a = __builtin_amdgcn_mfma_scale_f32_32x32x64_f8f6f4(kf8, qf8, a, 0, 0, 0, 0x797b, 1, 0x797b);
; #pragma unroll
;             for (int r = 0; r < 16; ++r) mx = fmaxf(mx, a[r]);
;             S[j] = a;
.LBB0_330:
	s_cmp_lt_i32 s9, 4
	s_cselect_b64 s[54:55], -1, 0
	s_cmp_gt_i32 s9, 3
	v_mov_b32_e32 v67, 0xff800000
	s_cbranch_scc1 .LBB0_336
	v_lshl_add_u32 v2, v118, 3, v118
	v_lshlrev_b32_e32 v2, 10, v2
	v_cmp_lt_i32_e32 vcc, -1, v117
	s_sub_i32 s0, s11, s10
	s_add_i32 s0, s0, 32
	v_cndmask_b32_e32 v2, 0, v2, vcc
	v_lshl_add_u64 v[52:53], v[112:113], 0, v[2:3]
	v_lshl_add_u32 v2, v120, 3, v120
	v_lshlrev_b32_e32 v2, 10, v2
	v_cmp_lt_i32_e32 vcc, -1, v119
	s_cmpk_lt_i32 s0, 0x81
	s_cselect_b64 s[0:1], -1, 0
	v_cndmask_b32_e32 v2, 0, v2, vcc
	v_lshl_add_u64 v[54:55], v[112:113], 0, v[2:3]
	global_load_dwordx4 v[68:71], v[52:53], off offset:1024
	global_load_dwordx4 v[72:75], v[54:55], off offset:1024
	v_add_u32_e32 v2, 32, v94
	v_cvt_f32_i32_e32 v2, v2
	s_cmp_gt_i32 s10, 31
	s_cselect_b64 s[56:57], -1, 0
	s_and_b64 s[56:57], s[56:57], s[0:1]
	v_sub_f32_e32 v2, v2, v115
	s_mov_b64 s[0:1], -1
	s_and_b64 vcc, exec, s[56:57]
	s_waitcnt vmcnt(3)
	ds_write_b128 v85, v[86:89]
	s_waitcnt vmcnt(2)
	ds_write_b128 v85, v[90:93] offset:1280
	s_cbranch_vccnz .LBB0_333
	s_brev_b32 s0, 1
	s_mov_b32 s1, -1.0
	v_pk_add_f32 v[52:53], v[2:3], s[0:1] op_sel_hi:[0,1]
	v_pk_mul_f32 v[54:55], v[98:99], v[52:53]
	v_cmp_le_f32_e64 vcc, |v52|, v115
	s_mov_b32 s0, -2.0
	s_mov_b32 s1, 0xc0400000
	v_cndmask_b32_e32 v52, v227, v54, vcc
	v_cmp_le_f32_e64 vcc, |v53|, v115
	s_nop 1
	v_cndmask_b32_e32 v53, v227, v55, vcc
	v_pk_add_f32 v[54:55], v[2:3], s[0:1] op_sel_hi:[0,1]
	v_pk_mul_f32 v[56:57], v[98:99], v[54:55]
	v_cmp_le_f32_e64 vcc, |v54|, v115
	s_mov_b32 s0, 0xc1000000
	s_mov_b32 s1, 0xc1100000
	v_cndmask_b32_e32 v54, v227, v56, vcc
	v_cmp_le_f32_e64 vcc, |v55|, v115
	s_nop 1
	v_cndmask_b32_e32 v55, v227, v57, vcc
	v_pk_add_f32 v[56:57], v[2:3], s[0:1] op_sel_hi:[0,1]
	v_pk_mul_f32 v[58:59], v[98:99], v[56:57]
	v_cmp_le_f32_e64 vcc, |v56|, v115
	s_mov_b32 s0, 0xc1200000
	s_mov_b32 s1, 0xc1300000
	v_cndmask_b32_e32 v56, v227, v58, vcc
	v_cmp_le_f32_e64 vcc, |v57|, v115
	s_nop 1
	v_cndmask_b32_e32 v57, v227, v59, vcc
	v_pk_add_f32 v[58:59], v[2:3], s[0:1] op_sel_hi:[0,1]
	v_pk_mul_f32 v[60:61], v[98:99], v[58:59]
	v_cmp_le_f32_e64 vcc, |v58|, v115
	s_mov_b32 s0, 0xc1800000
	s_mov_b32 s1, 0xc1880000
	v_cndmask_b32_e32 v58, v227, v60, vcc
	v_cmp_le_f32_e64 vcc, |v59|, v115
	s_nop 1
	v_cndmask_b32_e32 v59, v227, v61, vcc
	v_pk_add_f32 v[60:61], v[2:3], s[0:1] op_sel_hi:[0,1]
	v_pk_mul_f32 v[62:63], v[98:99], v[60:61]
	v_cmp_le_f32_e64 vcc, |v60|, v115
	s_mov_b32 s0, 0xc1900000
	s_mov_b32 s1, 0xc1980000
	v_cndmask_b32_e32 v60, v227, v62, vcc
	v_cmp_le_f32_e64 vcc, |v61|, v115
	s_nop 1
	v_cndmask_b32_e32 v61, v227, v63, vcc
	v_pk_add_f32 v[62:63], v[2:3], s[0:1] op_sel_hi:[0,1]
	v_pk_mul_f32 v[64:65], v[98:99], v[62:63]
	v_cmp_le_f32_e64 vcc, |v62|, v115
	s_mov_b32 s0, 0xc1c00000
	s_mov_b32 s1, 0xc1c80000
	v_cndmask_b32_e32 v62, v227, v64, vcc
	v_cmp_le_f32_e64 vcc, |v63|, v115
	s_nop 1
	v_cndmask_b32_e32 v63, v227, v65, vcc
	v_pk_add_f32 v[64:65], v[2:3], s[0:1] op_sel_hi:[0,1]
	v_pk_mul_f32 v[66:67], v[98:99], v[64:65]
	v_cmp_le_f32_e64 vcc, |v64|, v115
	s_mov_b32 s0, 0xc1d00000
	s_mov_b32 s1, 0xc1d80000
	v_cndmask_b32_e32 v64, v227, v66, vcc
	v_cmp_le_f32_e64 vcc, |v65|, v115
	s_nop 1
	v_cndmask_b32_e32 v65, v227, v67, vcc
	v_pk_add_f32 v[66:67], v[2:3], s[0:1] op_sel_hi:[0,1]
	v_pk_mul_f32 v[76:77], v[98:99], v[66:67]
	v_cmp_le_f32_e64 vcc, |v66|, v115
	s_mov_b64 s[0:1], 0
	s_nop 0
	v_cndmask_b32_e32 v66, v227, v76, vcc
	v_cmp_le_f32_e64 vcc, |v67|, v115
	s_nop 1
	v_cndmask_b32_e32 v67, v227, v77, vcc

; #define AT_LOADROWS(dst, l0, ls, col) do { _Pragma("unroll") for (int i_ = 0; i_ < 2; ++i_) { int l_ = (l0) + (ls) * (16 * i_ + lr); l_ = l_ < 0 ? 0 : (l_ > L - 1 ? L - 1 : l_); \
;         dst[i_] = *(const GAS u32x4*)(base + (size_t)l_ * rstride + (col)); } } while (0)
; #define AT_PUTRAW(src) do { _Pragma("unroll") for (int i_ = 0; i_ < 2; ++i_) *(LAS u32x4*)(stg + (16 * i_ + lr) * 80 + lc * 16) = src[i_]; } while (0)
; template <bool FIRST, int NB> ...
;     ...
;     for (int j = 0; j < NB; ++j) {
;         if (j >= jlo) {
;             asm volatile("" ::: "memory");
;             if (j < NB - 1) AT_LOADROWS(kr[(j + 1) & 1], kb0 + 32 * (j + 1), 1, kcol);
;             AT_PUTRAW(kr[j & 1]);
;             const float xd0 = (float)(qpos - kb0 - 32 * j - 4 * hi) - half;
;             const bool inner = (q0 - kb0 - 32 * j - 31 >= 0) && (q0 + QS * 31 - kb0 - 32 * j <= 128) && (kb0 + 32 * j >= 0);
;             f32x16 a;
;             if (inner) {
;                 const float cb = -slope2d * xd0;
; #pragma unroll
;                 for (int r = 0; r < 16; ++r) a[r] = __builtin_fmaf(slope2d, (float)((r & 3) + 8 * (r >> 2)), cb);
;             } else {
.LBB0_337:
	s_cmp_lt_i32 s9, 5
	v_add_u32_e32 v146, 0xa0, v131
	v_add_u32_e32 v148, 0xb0, v131
	v_mov_b32_e32 v83, 0xff800000
	s_cselect_b64 s[56:57], -1, 0
	s_cmp_gt_i32 s9, 4
	v_min_i32_e32 v147, 0x7ff, v146
	v_cmp_lt_i32_e64 s[0:1], -1, v146
	v_min_i32_e32 v149, 0x7ff, v148
	v_cmp_lt_i32_e32 vcc, -1, v148
	s_cbranch_scc1 .LBB0_340
	v_lshl_add_u32 v2, v147, 3, v147
	v_lshlrev_b32_e32 v2, 10, v2
	v_cndmask_b32_e64 v2, 0, v2, s[0:1]
	v_lshl_add_u64 v[76:77], v[112:113], 0, v[2:3]
	v_lshl_add_u32 v2, v149, 3, v149
	v_lshlrev_b32_e32 v2, 10, v2
	v_cndmask_b32_e32 v2, 0, v2, vcc
	v_lshl_add_u64 v[78:79], v[112:113], 0, v[2:3]
	global_load_dwordx4 v[86:89], v[76:77], off offset:1024
	global_load_dwordx4 v[90:93], v[78:79], off offset:1024
	s_sub_i32 s0, s2, s10
	s_cmp_lt_i32 s0, 31
	s_cselect_b64 s[2:3], -1, 0
	s_and_b64 vcc, exec, s[2:3]
	s_waitcnt vmcnt(3)
	ds_write_b128 v85, v[68:71]
	s_waitcnt vmcnt(2)
	ds_write_b128 v85, v[72:75] offset:1280
	s_cbranch_vccnz .LBB0_341
	s_sub_i32 s0, s11, s10
	s_cmpk_gt_i32 s0, 0x80
	s_cselect_b64 s[0:1], -1, 0
	s_cmp_lt_i32 s10, 0
	s_cselect_b64 s[2:3], -1, 0
	s_or_b64 s[2:3], s[2:3], s[0:1]
	s_mov_b64 s[0:1], -1
	v_cvt_f32_i32_e32 v2, v94
	s_andn2_b64 vcc, exec, s[2:3]
	v_sub_f32_e32 v2, v2, v115
	s_cbranch_vccnz .LBB0_343
	s_branch .LBB0_342

; #define AT_LOADROWS(dst, l0, ls, col) do { _Pragma("unroll") for (int i_ = 0; i_ < 2; ++i_) { int l_ = (l0) + (ls) * (16 * i_ + lr); l_ = l_ < 0 ? 0 : (l_ > L - 1 ? L - 1 : l_); \
;         dst[i_] = *(const GAS u32x4*)(base + (size_t)l_ * rstride + (col)); } } while (0)
; template <bool FIRST, int NB> ...
;     ...
;     u32x4 vr[2][2];
; #pragma unroll
;     for (int j = 0; j < NB; ++j) if (j == jlo) AT_LOADROWS(vr[j & 1], kb0 + 32 * j, 1, vcol);
.LBB0_351:
	v_lshl_add_u32 v2, v122, 3, v122
	v_lshlrev_b32_e32 v2, 10, v2
	v_cmp_lt_i32_e32 vcc, -1, v121
	s_nop 1
	v_cndmask_b32_e32 v2, 0, v2, vcc
	s_waitcnt vmcnt(0) lgkmcnt(1)
	v_lshl_add_u64 v[100:101], v[112:113], 0, v[2:3]
	v_lshl_add_u32 v2, v124, 3, v124
	v_lshlrev_b32_e32 v2, 10, v2
	v_cmp_lt_i32_e32 vcc, -1, v123
	s_nop 1
	v_cndmask_b32_e32 v2, 0, v2, vcc
	v_lshl_add_u64 v[102:103], v[112:113], 0, v[2:3]
	s_waitcnt lgkmcnt(0)
	global_load_dwordx4 v[104:107], v[100:101], off offset:2048
	s_nop 0
	global_load_dwordx4 v[100:103], v[102:103], off offset:2048
	s_andn2_b64 vcc, exec, s[50:51]
	s_cbranch_vccz .LBB0_354
	s_branch .LBB0_355
.LBB0_352:
	v_min_i32_e32 v2, 0x7ff, v131
	v_lshl_add_u32 v2, v2, 3, v2
	v_lshlrev_b32_e32 v2, 10, v2
	v_cmp_lt_i32_e32 vcc, -1, v131
	s_nop 1
	v_cndmask_b32_e32 v2, 0, v2, vcc
	s_waitcnt lgkmcnt(1)
	v_lshl_add_u64 v[100:101], v[112:113], 0, v[2:3]
	v_add_u32_e32 v2, 16, v131
	v_min_i32_e32 v102, 0x7ff, v2
	v_lshl_add_u32 v102, v102, 3, v102
	v_lshlrev_b32_e32 v102, 10, v102
	v_cmp_lt_i32_e32 vcc, -1, v2
	s_nop 1
	v_cndmask_b32_e32 v2, 0, v102, vcc
	v_lshl_add_u64 v[102:103], v[112:113], 0, v[2:3]
	s_waitcnt lgkmcnt(0)
	global_load_dwordx4 v[104:107], v[100:101], off offset:2048
	s_nop 0
	global_load_dwordx4 v[100:103], v[102:103], off offset:2048
	s_andn2_b64 vcc, exec, s[48:49]
	s_cbranch_vccz .LBB0_351

; __device__ __forceinline__ unsigned cvt_pk_bf16(float lo, float hi) { return pk2(lo, hi); }
; #define AT_LOADROWS(dst, l0, ls, col) do { _Pragma("unroll") for (int i_ = 0; i_ < 2; ++i_) { int l_ = (l0) + (ls) * (16 * i_ + lr); l_ = l_ < 0 ? 0 : (l_ > L - 1 ? L - 1 : l_); \
;         dst[i_] = *(const GAS u32x4*)(base + (size_t)l_ * rstride + (col)); } } while (0)
; template <bool FIRST, int NB> ...
;     ...
;     u32x4 vr[2][2];
; #pragma unroll
;     for (int j = 0; j < NB; ++j) if (j == jlo) AT_LOADROWS(vr[j & 1], kb0 + 32 * j, 1, vcol);
;     { auto rr = __builtin_amdgcn_permlane32_swap(__float_as_uint(mx), __float_as_uint(mx), false, false);
;       const unsigned r0 = rr[0], r1 = rr[1]; mx = fmaxf(__uint_as_float(r0), __uint_as_float(r1)); }
;     const float mx_true = mx - slope2d * half;
;     float lsum = 0.f;
;     u32x4 P[NB][2];
; #pragma unroll
;     for (int j = 0; j < NB; ++j) {
;         float p[16];
; #pragma unroll
;         for (int r = 0; r < 16; ++r) { p[r] = __builtin_amdgcn_exp2f(S[j][r] - mx); lsum += p[r]; }
; #pragma unroll
;         for (int ks = 0; ks < 2; ++ks) { P[j][ks].x = cvt_pk_bf16(p[8 * ks + 0], p[8 * ks + 1]); P[j][ks].y = cvt_pk_bf16(p[8 * ks + 2], p[8 * ks + 3]); P[j][ks].z = cvt_pk_bf16(p[8 * ks + 4], p[8 * ks + 5]); P[j][ks].w = cvt_pk_bf16(p[8 * ks + 6], p[8 * ks + 7]); }
;         __builtin_amdgcn_sched_barrier(0);
;     }
.LBB0_354:
	v_lshl_add_u32 v2, v118, 3, v118
	v_lshlrev_b32_e32 v2, 10, v2
	v_cmp_lt_i32_e32 vcc, -1, v117
	s_nop 1
	v_cndmask_b32_e32 v2, 0, v2, vcc
	s_waitcnt vmcnt(0) lgkmcnt(1)
	v_lshl_add_u64 v[100:101], v[112:113], 0, v[2:3]
	v_lshl_add_u32 v2, v120, 3, v120
	v_lshlrev_b32_e32 v2, 10, v2
	v_cmp_lt_i32_e32 vcc, -1, v119
	s_nop 1
	v_cndmask_b32_e32 v2, 0, v2, vcc
	v_lshl_add_u64 v[102:103], v[112:113], 0, v[2:3]
	s_waitcnt lgkmcnt(0)
	global_load_dwordx4 v[104:107], v[100:101], off offset:2048
	s_nop 0
	global_load_dwordx4 v[100:103], v[102:103], off offset:2048
.LBB0_355:
	v_mov_b32_e32 v2, v150
	s_nop 1
	v_permlane32_swap_b32_e32 v150, v2
	v_max_f32_e32 v2, v2, v2
	v_max_f32_e32 v131, v150, v150
	v_max_f32_e32 v131, v131, v2
	v_sub_f32_e32 v2, v4, v131
	v_exp_f32_e32 v2, v2
	v_sub_f32_e32 v4, v5, v131
	v_exp_f32_e32 v4, v4
	v_sub_f32_e32 v5, v6, v131
	v_exp_f32_e32 v5, v5
	v_sub_f32_e32 v6, v7, v131
	v_exp_f32_e32 v6, v6
	v_sub_f32_e32 v7, v8, v131
	v_exp_f32_e32 v7, v7
	v_sub_f32_e32 v8, v9, v131
	v_sub_f32_e32 v9, v10, v131
	v_sub_f32_e32 v10, v11, v131
	v_sub_f32_e32 v11, v12, v131
	v_sub_f32_e32 v12, v13, v131
	v_sub_f32_e32 v13, v14, v131
	v_sub_f32_e32 v14, v15, v131
	v_sub_f32_e32 v15, v16, v131
	v_sub_f32_e32 v16, v17, v131
	v_sub_f32_e32 v17, v18, v131
	v_sub_f32_e32 v18, v19, v131
	v_add_f32_e32 v19, 0, v2
	v_exp_f32_e32 v8, v8
	v_add_f32_e32 v19, v4, v19
	v_exp_f32_e32 v9, v9
	v_add_f32_e32 v19, v5, v19
	v_exp_f32_e32 v10, v10
	v_add_f32_e32 v19, v6, v19
	v_exp_f32_e32 v11, v11
	v_add_f32_e32 v19, v7, v19
	v_exp_f32_e32 v12, v12
	v_add_f32_e32 v19, v8, v19
	v_exp_f32_e32 v13, v13
	v_add_f32_e32 v19, v9, v19
	v_exp_f32_e32 v14, v14
	v_add_f32_e32 v19, v10, v19
	v_exp_f32_e32 v15, v15
	v_add_f32_e32 v19, v11, v19
	v_exp_f32_e32 v16, v16
	v_add_f32_e32 v19, v12, v19
	v_exp_f32_e32 v17, v17
	v_add_f32_e32 v19, v13, v19
	v_exp_f32_e32 v18, v18
	v_add_f32_e32 v19, v14, v19
	v_add_f32_e32 v19, v15, v19
	v_add_f32_e32 v19, v16, v19
	v_add_f32_e32 v19, v17, v19
	v_add_u32_e32 v204, 16, v125
	v_add_f32_e32 v19, v18, v19
	v_sub_f32_e32 v20, v20, v131
	v_exp_f32_e32 v188, v20
	v_sub_f32_e32 v20, v21, v131
	v_exp_f32_e32 v189, v20
	v_sub_f32_e32 v20, v22, v131
	v_exp_f32_e32 v190, v20
	v_sub_f32_e32 v20, v23, v131
	v_exp_f32_e32 v191, v20
	v_sub_f32_e32 v20, v24, v131
	v_exp_f32_e32 v192, v20
	v_sub_f32_e32 v20, v25, v131
	v_add_f32_e32 v19, v188, v19
	v_exp_f32_e32 v193, v20
	v_sub_f32_e32 v20, v26, v131
	v_add_f32_e32 v19, v189, v19
	v_exp_f32_e32 v194, v20
	v_sub_f32_e32 v20, v27, v131
	v_add_f32_e32 v19, v190, v19
	v_exp_f32_e32 v195, v20
	v_sub_f32_e32 v20, v28, v131
	v_add_f32_e32 v19, v191, v19
	v_exp_f32_e32 v196, v20
	v_sub_f32_e32 v20, v29, v131
	v_add_f32_e32 v19, v192, v19
	v_exp_f32_e32 v197, v20
	v_sub_f32_e32 v20, v30, v131
	v_add_f32_e32 v19, v193, v19
	v_exp_f32_e32 v198, v20
	v_sub_f32_e32 v20, v31, v131
	v_add_f32_e32 v19, v194, v19
	v_exp_f32_e32 v199, v20
	v_sub_f32_e32 v20, v32, v131
	v_add_f32_e32 v19, v195, v19
	v_exp_f32_e32 v200, v20
	v_sub_f32_e32 v20, v33, v131
	v_add_f32_e32 v19, v196, v19
	v_exp_f32_e32 v201, v20
	v_sub_f32_e32 v20, v34, v131
	v_add_f32_e32 v19, v197, v19
	v_exp_f32_e32 v202, v20
	v_sub_f32_e32 v20, v35, v131
	v_add_f32_e32 v19, v198, v19
	v_exp_f32_e32 v203, v20
	v_add_f32_e32 v19, v199, v19
	v_add_f32_e32 v19, v200, v19
	v_add_f32_e32 v19, v201, v19
	v_add_f32_e32 v19, v202, v19
	v_add_f32_e32 v19, v203, v19
	v_sub_f32_e32 v20, v36, v131
	v_exp_f32_e32 v172, v20
	v_sub_f32_e32 v20, v37, v131
	v_exp_f32_e32 v173, v20
	v_sub_f32_e32 v20, v38, v131
	v_exp_f32_e32 v174, v20
	v_sub_f32_e32 v20, v39, v131
	v_exp_f32_e32 v175, v20
	v_sub_f32_e32 v20, v40, v131
	v_exp_f32_e32 v176, v20
	v_sub_f32_e32 v20, v41, v131
	v_add_f32_e32 v19, v172, v19
	v_exp_f32_e32 v177, v20
	v_sub_f32_e32 v20, v42, v131
	v_add_f32_e32 v19, v173, v19
	v_exp_f32_e32 v178, v20
	v_sub_f32_e32 v20, v43, v131
	v_add_f32_e32 v19, v174, v19
	v_exp_f32_e32 v179, v20
	v_sub_f32_e32 v20, v44, v131
	v_add_f32_e32 v19, v175, v19
	v_exp_f32_e32 v180, v20
	v_sub_f32_e32 v20, v45, v131
	v_add_f32_e32 v19, v176, v19
	v_exp_f32_e32 v181, v20
	v_sub_f32_e32 v20, v46, v131
	v_add_f32_e32 v19, v177, v19
	v_exp_f32_e32 v182, v20
	v_sub_f32_e32 v20, v47, v131
	v_add_f32_e32 v19, v178, v19
	v_exp_f32_e32 v183, v20
	v_sub_f32_e32 v20, v48, v131
	v_add_f32_e32 v19, v179, v19
	v_exp_f32_e32 v184, v20
	v_sub_f32_e32 v20, v49, v131
	v_add_f32_e32 v19, v180, v19
	v_exp_f32_e32 v185, v20
	v_sub_f32_e32 v20, v50, v131
	v_add_f32_e32 v19, v181, v19
	v_exp_f32_e32 v186, v20
	v_sub_f32_e32 v20, v51, v131
	v_add_f32_e32 v19, v182, v19
	v_exp_f32_e32 v187, v20
	v_add_f32_e32 v19, v183, v19
	v_add_f32_e32 v19, v184, v19
	v_add_f32_e32 v19, v185, v19
	v_add_f32_e32 v19, v186, v19
	v_add_f32_e32 v19, v187, v19
	v_sub_f32_e32 v20, v52, v131
	v_exp_f32_e32 v156, v20
	v_sub_f32_e32 v20, v53, v131
	v_exp_f32_e32 v157, v20
	v_sub_f32_e32 v20, v54, v131
	v_exp_f32_e32 v158, v20
	v_sub_f32_e32 v20, v55, v131
	v_exp_f32_e32 v159, v20
	v_sub_f32_e32 v20, v56, v131
	v_exp_f32_e32 v160, v20
	v_sub_f32_e32 v20, v57, v131
	v_add_f32_e32 v19, v156, v19
	v_exp_f32_e32 v161, v20
	v_sub_f32_e32 v20, v58, v131
	v_add_f32_e32 v19, v157, v19
	v_exp_f32_e32 v162, v20
	v_sub_f32_e32 v20, v59, v131
	v_add_f32_e32 v19, v158, v19
	v_exp_f32_e32 v163, v20
	v_sub_f32_e32 v20, v60, v131
	v_add_f32_e32 v19, v159, v19
	v_exp_f32_e32 v164, v20
	v_sub_f32_e32 v20, v61, v131
	v_add_f32_e32 v19, v160, v19
	v_exp_f32_e32 v165, v20
	v_sub_f32_e32 v20, v62, v131
	v_add_f32_e32 v19, v161, v19
	v_exp_f32_e32 v166, v20
	v_sub_f32_e32 v20, v63, v131
	v_add_f32_e32 v19, v162, v19
; template <bool FIRST, int NB> ...
;     ...
; #pragma unroll
;     for (int j = 0; j < NB; ++j) {
;         float p[16];
; #pragma unroll
;         for (int r = 0; r < 16; ++r) { p[r] = __builtin_amdgcn_exp2f(S[j][r] - mx); lsum += p[r]; }
; #pragma unroll
;         for (int ks = 0; ks < 2; ++ks) { P[j][ks].x = cvt_pk_bf16(p[8 * ks + 0], p[8 * ks + 1]); P[j][ks].y = cvt_pk_bf16(p[8 * ks + 2], p[8 * ks + 3]); P[j][ks].z = cvt_pk_bf16(p[8 * ks + 4], p[8 * ks + 5]); P[j][ks].w = cvt_pk_bf16(p[8 * ks + 6], p[8 * ks + 7]); }
;         __builtin_amdgcn_sched_barrier(0);
;     }
;     { auto rr = __builtin_amdgcn_permlane32_swap(__float_as_uint(lsum), __float_as_uint(lsum), false, false);
;       const unsigned r0 = rr[0], r1 = rr[1]; lsum = __uint_as_float(r0) + __uint_as_float(r1); }
;     f32x16 o[2]; o[0] = (f32x16){}; o[1] = (f32x16){};
;     const unsigned vrd = (unsigned)(((lane >> 4) & 1) * 32 + (lane & 3) * 8 + (4 * hi + ((lane & 15) >> 2)) * 64);
; #pragma unroll
;     for (int j = 0; j < NB; ++j) {
;         if (j >= jlo) {
;             asm volatile("" ::: "memory");
;             if (j < NB - 1) AT_LOADROWS(vr[(j + 1) & 1], kb0 + 32 * (j + 1), 1, vcol);
; #pragma unroll
;             for (int i = 0; i < 2; ++i) { const int key = 16 * i + lr;
; #pragma unroll
;                 for (int hf = 0; hf < 2; ++hf) { const int c8 = 2 * lc + hf; const u32x4 src = vr[j & 1][i];
;                     *(LAS u32x4*)(stg + ((c8 >> 2) * 2 + (key >> 4)) * 1024 + (key & 15) * 64 + (c8 & 3) * 16) = f8x8_to_bf16(hf ? src.z : src.x, hf ? src.w : src.y, 1.0f / 16.0f); } }
;             AT_LDSWAIT();
; #pragma unroll
;             for (int d0 = 0; d0 < 2; ++d0)
; #pragma unroll
;                 for (int ks = 0; ks < 2; ++ks) {
;                     LAS unsigned char* vp = stg + (d0 * 2 + ks) * 1024 + vrd;
;                     const s16x4 lo = __builtin_bit_cast(s16x4, __builtin_amdgcn_ds_read_tr16_b64_v4i16((LAS s16x4*)(vp)));
;                     const s16x4 hh = __builtin_bit_cast(s16x4, __builtin_amdgcn_ds_read_tr16_b64_v4i16((LAS s16x4*)(vp + 512)));
;                     const bf16x8 vf = (bf16x8){lo[0], lo[1], lo[2], lo[3], hh[0], hh[1], hh[2], hh[3]};
;                     o[d0] = MFMA32(__builtin_bit_cast(bf16x8, P[j][ks]), vf, o[d0]);
;                 }
;             AT_LDSWAIT();
;         }
;         __builtin_amdgcn_sched_barrier(0);
;     }
	v_exp_f32_e32 v167, v20
	v_sub_f32_e32 v20, v64, v131
	v_add_f32_e32 v19, v163, v19
	v_exp_f32_e32 v168, v20
	v_sub_f32_e32 v20, v65, v131
	v_add_f32_e32 v19, v164, v19
	v_exp_f32_e32 v169, v20
	v_sub_f32_e32 v20, v66, v131
	v_add_f32_e32 v19, v165, v19
	v_exp_f32_e32 v170, v20
	v_sub_f32_e32 v20, v67, v131
	v_add_f32_e32 v19, v166, v19
	v_exp_f32_e32 v171, v20
	v_add_f32_e32 v19, v167, v19
	v_add_f32_e32 v19, v168, v19
	v_add_f32_e32 v19, v169, v19
	v_add_f32_e32 v19, v170, v19
	v_add_f32_e32 v19, v171, v19
	v_sub_f32_e32 v20, v68, v131
	v_exp_f32_e32 v145, v20
	v_sub_f32_e32 v20, v69, v131
	v_exp_f32_e32 v150, v20
	v_sub_f32_e32 v20, v70, v131
	v_exp_f32_e32 v151, v20
	v_sub_f32_e32 v20, v71, v131
	v_exp_f32_e32 v152, v20
	v_sub_f32_e32 v20, v72, v131
	v_exp_f32_e32 v153, v20
	v_sub_f32_e32 v20, v73, v131
	v_add_f32_e32 v19, v145, v19
	v_exp_f32_e32 v154, v20
	v_sub_f32_e32 v20, v74, v131
	v_add_f32_e32 v19, v150, v19
	v_exp_f32_e32 v155, v20
	v_sub_f32_e32 v20, v75, v131
	v_add_f32_e32 v19, v151, v19
	v_exp_f32_e32 v75, v20
	v_sub_f32_e32 v20, v76, v131
	v_add_f32_e32 v19, v152, v19
	v_exp_f32_e32 v70, v20
	v_sub_f32_e32 v20, v77, v131
	v_add_f32_e32 v19, v153, v19
	v_exp_f32_e32 v72, v20
	v_sub_f32_e32 v20, v78, v131
	v_add_f32_e32 v19, v154, v19
	v_exp_f32_e32 v64, v20
	v_sub_f32_e32 v20, v79, v131
	v_add_f32_e32 v19, v155, v19
	v_exp_f32_e32 v66, v20
	v_sub_f32_e32 v20, v80, v131
	v_add_f32_e32 v19, v75, v19
	v_exp_f32_e32 v67, v20
	v_sub_f32_e32 v20, v81, v131
	v_add_f32_e32 v19, v70, v19
	v_exp_f32_e32 v68, v20
	v_sub_f32_e32 v20, v82, v131
	v_add_f32_e32 v19, v72, v19
	v_exp_f32_e32 v71, v20
	v_sub_f32_e32 v20, v83, v131
	v_add_f32_e32 v19, v64, v19
	v_exp_f32_e32 v73, v20
	v_add_f32_e32 v19, v66, v19
	v_add_f32_e32 v19, v67, v19
	v_add_f32_e32 v19, v68, v19
	v_add_f32_e32 v19, v71, v19
	v_add_f32_e32 v19, v73, v19
	v_sub_f32_e32 v20, v84, v131
	v_exp_f32_e32 v55, v20
	v_sub_f32_e32 v20, v85, v131
	v_exp_f32_e32 v56, v20
	v_sub_f32_e32 v20, v86, v131
	v_exp_f32_e32 v57, v20
	v_sub_f32_e32 v20, v87, v131
	v_exp_f32_e32 v58, v20
	v_sub_f32_e32 v20, v88, v131
	v_exp_f32_e32 v59, v20
	v_sub_f32_e32 v20, v89, v131
	v_add_f32_e32 v19, v55, v19
	v_exp_f32_e32 v60, v20
	v_sub_f32_e32 v20, v90, v131
	v_add_f32_e32 v19, v56, v19
	v_exp_f32_e32 v61, v20
	v_sub_f32_e32 v20, v91, v131
	v_add_f32_e32 v19, v57, v19
	v_exp_f32_e32 v62, v20
	v_sub_f32_e32 v20, v92, v131
	v_add_f32_e32 v19, v58, v19
	v_exp_f32_e32 v50, v20
	v_sub_f32_e32 v20, v93, v131
	v_add_f32_e32 v19, v59, v19
	v_exp_f32_e32 v52, v20
	v_sub_f32_e32 v20, v94, v131
	v_add_f32_e32 v19, v60, v19
	v_exp_f32_e32 v46, v20
	v_sub_f32_e32 v20, v95, v131
	v_add_f32_e32 v19, v61, v19
	v_exp_f32_e32 v47, v20
	v_sub_f32_e32 v20, v96, v131
	v_add_f32_e32 v19, v62, v19
	v_exp_f32_e32 v48, v20
	v_sub_f32_e32 v20, v97, v131
	v_add_f32_e32 v19, v50, v19
	v_exp_f32_e32 v49, v20
	v_sub_f32_e32 v20, v98, v131
	v_add_f32_e32 v19, v52, v19
	v_exp_f32_e32 v51, v20
	v_sub_f32_e32 v20, v99, v131
	v_add_f32_e32 v19, v46, v19
	v_exp_f32_e32 v53, v20
	v_add_f32_e32 v19, v47, v19
	v_add_f32_e32 v19, v48, v19
	v_add_f32_e32 v19, v49, v19
	v_add_f32_e32 v19, v51, v19
	v_add_f32_e32 v44, v53, v19
	v_lshlrev_b32_e32 v19, 1, v114
	v_lshrrev_b32_e32 v21, 2, v114
	v_lshlrev_b32_e32 v22, 1, v126
	v_and_b32_e32 v19, 32, v19
	v_lshlrev_b32_e32 v20, 3, v126
	v_and_or_b32 v21, v21, 3, v116
	v_lshlrev_b32_e32 v24, 6, v125
	v_and_b32_e32 v22, 2, v22
	v_mov_b32_e32 v45, v44
	v_lshlrev_b32_e32 v21, 6, v21
	v_and_b32_e32 v23, 2, v114
	v_and_b32_e32 v24, 0x3c0, v24
	v_add3_u32 v19, s77, v19, v20
	v_lshrrev_b32_e32 v20, 6, v114
	v_lshlrev_b32_e32 v65, 4, v22
	v_lshrrev_b32_e32 v22, 4, v204
	v_permlane32_swap_b32_e32 v44, v45
	v_add_u32_e32 v63, s77, v24
	s_andn2_b64 vcc, exec, s[42:43]
	v_add_u32_e32 v54, v19, v21
	v_add_lshl_u32 v74, v20, v23, 10
	v_add_lshl_u32 v69, v22, v23, 10
	s_cbranch_vccnz .LBB0_357
	v_cvt_pk_bf16_f32 v20, v2, v4
	v_lshl_add_u32 v2, v130, 3, v130
	v_lshlrev_b32_e32 v2, 10, v2
	v_cmp_lt_i32_e32 vcc, -1, v129
	v_cvt_pk_bf16_f32 v21, v5, v6
	v_cvt_pk_bf16_f32 v22, v7, v8
	v_cndmask_b32_e32 v2, 0, v2, vcc
	v_lshl_add_u64 v[4:5], v[112:113], 0, v[2:3]
	v_lshl_add_u32 v2, v128, 3, v128
	v_lshlrev_b32_e32 v2, 10, v2
	v_cmp_lt_i32_e32 vcc, -1, v127
	global_load_dwordx4 v[36:39], v[4:5], off offset:2048
	s_waitcnt vmcnt(2) lgkmcnt(0)
	v_cvt_scalef32_pk_bf16_fp8 v6, v105, s80
	v_cndmask_b32_e32 v2, 0, v2, vcc
	v_lshl_add_u64 v[4:5], v[112:113], 0, v[2:3]
	global_load_dwordx4 v[40:43], v[4:5], off offset:2048
	v_cvt_scalef32_pk_bf16_fp8 v4, v104, s80
	v_cvt_scalef32_pk_bf16_fp8 v5, v104, s80 op_sel:[1,0,0]
	v_cvt_scalef32_pk_bf16_fp8 v7, v105, s80 op_sel:[1,0,0]
	v_add3_u32 v2, v63, v74, v65
	ds_write_b128 v2, v[4:7]
	v_cvt_scalef32_pk_bf16_fp8 v4, v106, s80
	v_cvt_scalef32_pk_bf16_fp8 v5, v106, s80 op_sel:[1,0,0]
	v_cvt_scalef32_pk_bf16_fp8 v6, v107, s80
	v_cvt_scalef32_pk_bf16_fp8 v7, v107, s80 op_sel:[1,0,0]
	ds_write_b128 v2, v[4:7] offset:16
	s_waitcnt vmcnt(2)
	v_cvt_scalef32_pk_bf16_fp8 v4, v100, s80
	v_cvt_scalef32_pk_bf16_fp8 v5, v100, s80 op_sel:[1,0,0]
	v_cvt_scalef32_pk_bf16_fp8 v6, v101, s80
	v_cvt_scalef32_pk_bf16_fp8 v7, v101, s80 op_sel:[1,0,0]
	v_add3_u32 v2, v63, v69, v65
	ds_write_b128 v2, v[4:7]
	v_cvt_scalef32_pk_bf16_fp8 v4, v102, s80
	v_cvt_scalef32_pk_bf16_fp8 v5, v102, s80 op_sel:[1,0,0]
	v_cvt_scalef32_pk_bf16_fp8 v6, v103, s80
	v_cvt_scalef32_pk_bf16_fp8 v7, v103, s80 op_sel:[1,0,0]
	ds_write_b128 v2, v[4:7] offset:16
	s_waitcnt lgkmcnt(0)
	v_cvt_pk_bf16_f32 v23, v9, v10
	ds_read_b64_tr_b16 v[4:5], v54
	ds_read_b64_tr_b16 v[6:7], v54 offset:512
	v_cvt_pk_bf16_f32 v76, v11, v12
	v_cvt_pk_bf16_f32 v77, v13, v14
	v_cvt_pk_bf16_f32 v78, v15, v16
	v_cvt_pk_bf16_f32 v79, v17, v18
	s_waitcnt lgkmcnt(0)
	v_mfma_f32_32x32x16_bf16 v[4:19], v[20:23], v[4:7], 0
	ds_read_b64_tr_b16 v[24:25], v54 offset:1024
	ds_read_b64_tr_b16 v[26:27], v54 offset:1536
	s_waitcnt lgkmcnt(0)
	v_mfma_f32_32x32x16_bf16 v[4:19], v[76:79], v[24:27], v[4:19]
	ds_read_b64_tr_b16 v[24:25], v54 offset:2048
	ds_read_b64_tr_b16 v[26:27], v54 offset:2560
	ds_read_b64_tr_b16 v[80:81], v54 offset:3072
	ds_read_b64_tr_b16 v[82:83], v54 offset:3584
	s_waitcnt lgkmcnt(0)
	s_waitcnt lgkmcnt(2)
	v_mfma_f32_32x32x16_bf16 v[20:35], v[20:23], v[24:27], 0
	s_waitcnt lgkmcnt(0)
	v_mfma_f32_32x32x16_bf16 v[20:35], v[76:79], v[80:83], v[20:35]
	s_branch .LBB0_358

; #define LAS __attribute__((address_space(3)))
; #define MFMA32(a, b, c) __builtin_amdgcn_mfma_f32_32x32x16_bf16(a, b, c, 0, 0, 0)
; #define AT_LOADROWS(dst, l0, ls, col) do { _Pragma("unroll") for (int i_ = 0; i_ < 2; ++i_) { int l_ = (l0) + (ls) * (16 * i_ + lr); l_ = l_ < 0 ? 0 : (l_ > L - 1 ? L - 1 : l_); \
;         dst[i_] = *(const GAS u32x4*)(base + (size_t)l_ * rstride + (col)); } } while (0)
; #define AT_LDSWAIT() asm volatile("s_waitcnt lgkmcnt(0)" ::: "memory")
; template <bool FIRST, int NB> ...
;     ...
; #pragma unroll
;     for (int j = 0; j < NB; ++j) {
;         if (j >= jlo) {
;             asm volatile("" ::: "memory");
;             if (j < NB - 1) AT_LOADROWS(vr[(j + 1) & 1], kb0 + 32 * (j + 1), 1, vcol);
; #pragma unroll
;             for (int i = 0; i < 2; ++i) { const int key = 16 * i + lr;
; #pragma unroll
;                 for (int hf = 0; hf < 2; ++hf) { const int c8 = 2 * lc + hf; const u32x4 src = vr[j & 1][i];
;                     *(LAS u32x4*)(stg + ((c8 >> 2) * 2 + (key >> 4)) * 1024 + (key & 15) * 64 + (c8 & 3) * 16) = f8x8_to_bf16(hf ? src.z : src.x, hf ? src.w : src.y, 1.0f / 16.0f); } }
;             AT_LDSWAIT();
; #pragma unroll
;             for (int d0 = 0; d0 < 2; ++d0)
; #pragma unroll
;                 for (int ks = 0; ks < 2; ++ks) {
;                     LAS unsigned char* vp = stg + (d0 * 2 + ks) * 1024 + vrd;
;                     const s16x4 lo = __builtin_bit_cast(s16x4, __builtin_amdgcn_ds_read_tr16_b64_v4i16((LAS s16x4*)(vp)));
;                     const s16x4 hh = __builtin_bit_cast(s16x4, __builtin_amdgcn_ds_read_tr16_b64_v4i16((LAS s16x4*)(vp + 512)));
;                     const bf16x8 vf = (bf16x8){lo[0], lo[1], lo[2], lo[3], hh[0], hh[1], hh[2], hh[3]};
;                     o[d0] = MFMA32(__builtin_bit_cast(bf16x8, P[j][ks]), vf, o[d0]);
;                 }
;             AT_LDSWAIT();
;         }
;         __builtin_amdgcn_sched_barrier(0);
;     }
.LBB0_358:
	s_andn2_b64 vcc, exec, s[44:45]
	s_cbranch_vccnz .LBB0_360
	v_lshl_add_u32 v2, v124, 3, v124
	v_lshlrev_b32_e32 v2, 10, v2
	v_cmp_lt_i32_e32 vcc, -1, v123
	s_waitcnt vmcnt(0)
	v_cvt_scalef32_pk_bf16_fp8 v86, v41, s80
	v_cvt_scalef32_pk_bf16_fp8 v87, v41, s80 op_sel:[1,0,0]
	v_cndmask_b32_e32 v2, 0, v2, vcc
	v_lshl_add_u64 v[84:85], v[112:113], 0, v[2:3]
	v_lshl_add_u32 v2, v122, 3, v122
	v_lshlrev_b32_e32 v2, 10, v2
	v_cmp_lt_i32_e32 vcc, -1, v121
	s_waitcnt lgkmcnt(1)
	global_load_dwordx4 v[100:103], v[84:85], off offset:2048
	v_cvt_pk_bf16_f32 v76, v188, v189
	v_cndmask_b32_e32 v2, 0, v2, vcc
	v_lshl_add_u64 v[84:85], v[112:113], 0, v[2:3]
	s_waitcnt lgkmcnt(0)
	global_load_dwordx4 v[104:107], v[84:85], off offset:2048
	v_cvt_scalef32_pk_bf16_fp8 v84, v40, s80
	v_cvt_scalef32_pk_bf16_fp8 v85, v40, s80 op_sel:[1,0,0]
	v_add3_u32 v2, v63, v74, v65
	ds_write_b128 v2, v[84:87]
	v_cvt_scalef32_pk_bf16_fp8 v84, v42, s80
	v_cvt_scalef32_pk_bf16_fp8 v85, v42, s80 op_sel:[1,0,0]
	v_cvt_scalef32_pk_bf16_fp8 v86, v43, s80
	v_cvt_scalef32_pk_bf16_fp8 v87, v43, s80 op_sel:[1,0,0]
	ds_write_b128 v2, v[84:87] offset:16
	v_cvt_scalef32_pk_bf16_fp8 v84, v36, s80
	v_cvt_scalef32_pk_bf16_fp8 v85, v36, s80 op_sel:[1,0,0]
	v_cvt_scalef32_pk_bf16_fp8 v86, v37, s80
	v_cvt_scalef32_pk_bf16_fp8 v87, v37, s80 op_sel:[1,0,0]
	v_add3_u32 v2, v63, v69, v65
	ds_write_b128 v2, v[84:87]
	v_cvt_scalef32_pk_bf16_fp8 v84, v38, s80
	v_cvt_scalef32_pk_bf16_fp8 v85, v38, s80 op_sel:[1,0,0]
	v_cvt_scalef32_pk_bf16_fp8 v86, v39, s80
	v_cvt_scalef32_pk_bf16_fp8 v87, v39, s80 op_sel:[1,0,0]
	ds_write_b128 v2, v[84:87] offset:16
	s_waitcnt lgkmcnt(0)
	v_cvt_pk_bf16_f32 v77, v190, v191
	v_cvt_pk_bf16_f32 v78, v192, v193
	v_cvt_pk_bf16_f32 v79, v194, v195
	ds_read_b64_tr_b16 v[84:85], v54
	ds_read_b64_tr_b16 v[86:87], v54 offset:512
	s_waitcnt lgkmcnt(0)
	v_mfma_f32_32x32x16_bf16 v[4:19], v[76:79], v[84:87], v[4:19]
	v_cvt_pk_bf16_f32 v80, v196, v197
	v_cvt_pk_bf16_f32 v81, v198, v199
	v_cvt_pk_bf16_f32 v82, v200, v201
	v_cvt_pk_bf16_f32 v83, v202, v203
	ds_read_b64_tr_b16 v[84:85], v54 offset:1024
	ds_read_b64_tr_b16 v[86:87], v54 offset:1536
	s_waitcnt lgkmcnt(0)
	v_mfma_f32_32x32x16_bf16 v[4:19], v[80:83], v[84:87], v[4:19]
	ds_read_b64_tr_b16 v[84:85], v54 offset:2048
	ds_read_b64_tr_b16 v[86:87], v54 offset:2560
	s_waitcnt lgkmcnt(0)
	v_mfma_f32_32x32x16_bf16 v[20:35], v[76:79], v[84:87], v[20:35]
	ds_read_b64_tr_b16 v[76:77], v54 offset:3072
	ds_read_b64_tr_b16 v[78:79], v54 offset:3584
	s_waitcnt lgkmcnt(0)
	s_waitcnt lgkmcnt(0)
	v_mfma_f32_32x32x16_bf16 v[20:35], v[80:83], v[76:79], v[20:35]
.LBB0_360:
	s_andn2_b64 vcc, exec, s[52:53]
	s_cbranch_vccnz .LBB0_362
	v_lshl_add_u32 v2, v144, 3, v144
	v_lshlrev_b32_e32 v2, 10, v2
	v_cmp_lt_i32_e32 vcc, -1, v143
	s_waitcnt vmcnt(0) lgkmcnt(0)
	v_cvt_scalef32_pk_bf16_fp8 v84, v104, s80
	v_cvt_scalef32_pk_bf16_fp8 v85, v104, s80 op_sel:[1,0,0]
	v_cndmask_b32_e32 v2, 0, v2, vcc
	v_lshl_add_u64 v[36:37], v[112:113], 0, v[2:3]
	v_lshl_add_u32 v2, v133, 3, v133
	v_lshlrev_b32_e32 v2, 10, v2
	v_cmp_lt_i32_e32 vcc, -1, v132
	global_load_dwordx4 v[36:39], v[36:37], off offset:2048
	v_cvt_scalef32_pk_bf16_fp8 v86, v105, s80
	v_cndmask_b32_e32 v2, 0, v2, vcc
	v_lshl_add_u64 v[40:41], v[112:113], 0, v[2:3]
	global_load_dwordx4 v[40:43], v[40:41], off offset:2048
	v_cvt_scalef32_pk_bf16_fp8 v87, v105, s80 op_sel:[1,0,0]
	v_add3_u32 v2, v63, v74, v65
	ds_write_b128 v2, v[84:87]
	v_cvt_scalef32_pk_bf16_fp8 v84, v106, s80
	v_cvt_scalef32_pk_bf16_fp8 v85, v106, s80 op_sel:[1,0,0]
	v_cvt_scalef32_pk_bf16_fp8 v86, v107, s80
	v_cvt_scalef32_pk_bf16_fp8 v87, v107, s80 op_sel:[1,0,0]
	ds_write_b128 v2, v[84:87] offset:16
	v_cvt_scalef32_pk_bf16_fp8 v84, v100, s80
	v_cvt_scalef32_pk_bf16_fp8 v85, v100, s80 op_sel:[1,0,0]
	v_cvt_scalef32_pk_bf16_fp8 v86, v101, s80
	v_cvt_scalef32_pk_bf16_fp8 v87, v101, s80 op_sel:[1,0,0]
	v_add3_u32 v2, v63, v69, v65
	ds_write_b128 v2, v[84:87]
	v_cvt_scalef32_pk_bf16_fp8 v84, v102, s80
	v_cvt_scalef32_pk_bf16_fp8 v85, v102, s80 op_sel:[1,0,0]
	v_cvt_scalef32_pk_bf16_fp8 v86, v103, s80
	v_cvt_scalef32_pk_bf16_fp8 v87, v103, s80 op_sel:[1,0,0]
	ds_write_b128 v2, v[84:87] offset:16
	s_waitcnt lgkmcnt(0)
	v_cvt_pk_bf16_f32 v76, v172, v173
	v_cvt_pk_bf16_f32 v77, v174, v175
	v_cvt_pk_bf16_f32 v78, v176, v177
	v_cvt_pk_bf16_f32 v79, v178, v179
	ds_read_b64_tr_b16 v[84:85], v54
	ds_read_b64_tr_b16 v[86:87], v54 offset:512
	s_waitcnt lgkmcnt(0)
	v_mfma_f32_32x32x16_bf16 v[4:19], v[76:79], v[84:87], v[4:19]
	v_cvt_pk_bf16_f32 v80, v180, v181
	v_cvt_pk_bf16_f32 v81, v182, v183
	v_cvt_pk_bf16_f32 v82, v184, v185
	v_cvt_pk_bf16_f32 v83, v186, v187
	ds_read_b64_tr_b16 v[84:85], v54 offset:1024
	ds_read_b64_tr_b16 v[86:87], v54 offset:1536
	s_waitcnt lgkmcnt(0)
	v_mfma_f32_32x32x16_bf16 v[4:19], v[80:83], v[84:87], v[4:19]
	ds_read_b64_tr_b16 v[84:85], v54 offset:2048
	ds_read_b64_tr_b16 v[86:87], v54 offset:2560
	s_waitcnt lgkmcnt(0)
	v_mfma_f32_32x32x16_bf16 v[20:35], v[76:79], v[84:87], v[20:35]
	ds_read_b64_tr_b16 v[76:77], v54 offset:3072
	ds_read_b64_tr_b16 v[78:79], v54 offset:3584
	s_waitcnt lgkmcnt(0)
	s_waitcnt lgkmcnt(0)
	v_mfma_f32_32x32x16_bf16 v[20:35], v[80:83], v[76:79], v[20:35]
; #define LAS __attribute__((address_space(3)))
; #define MFMA32(a, b, c) __builtin_amdgcn_mfma_f32_32x32x16_bf16(a, b, c, 0, 0, 0)
; #define AT_LOADROWS(dst, l0, ls, col) do { _Pragma("unroll") for (int i_ = 0; i_ < 2; ++i_) { int l_ = (l0) + (ls) * (16 * i_ + lr); l_ = l_ < 0 ? 0 : (l_ > L - 1 ? L - 1 : l_); \
;         dst[i_] = *(const GAS u32x4*)(base + (size_t)l_ * rstride + (col)); } } while (0)
; #define AT_LDSWAIT() asm volatile("s_waitcnt lgkmcnt(0)" ::: "memory")
; template <bool FIRST, int NB> ...
;     ...
; #pragma unroll
;     for (int j = 0; j < NB; ++j) {
;         if (j >= jlo) {
;             asm volatile("" ::: "memory");
;             if (j < NB - 1) AT_LOADROWS(vr[(j + 1) & 1], kb0 + 32 * (j + 1), 1, vcol);
; #pragma unroll
;             for (int i = 0; i < 2; ++i) { const int key = 16 * i + lr;
; #pragma unroll
;                 for (int hf = 0; hf < 2; ++hf) { const int c8 = 2 * lc + hf; const u32x4 src = vr[j & 1][i];
;                     *(LAS u32x4*)(stg + ((c8 >> 2) * 2 + (key >> 4)) * 1024 + (key & 15) * 64 + (c8 & 3) * 16) = f8x8_to_bf16(hf ? src.z : src.x, hf ? src.w : src.y, 1.0f / 16.0f); } }
;             AT_LDSWAIT();
; #pragma unroll
;             for (int d0 = 0; d0 < 2; ++d0)
; #pragma unroll
;                 for (int ks = 0; ks < 2; ++ks) {
;                     LAS unsigned char* vp = stg + (d0 * 2 + ks) * 1024 + vrd;
;                     const s16x4 lo = __builtin_bit_cast(s16x4, __builtin_amdgcn_ds_read_tr16_b64_v4i16((LAS s16x4*)(vp)));
;                     const s16x4 hh = __builtin_bit_cast(s16x4, __builtin_amdgcn_ds_read_tr16_b64_v4i16((LAS s16x4*)(vp + 512)));
;                     const bf16x8 vf = (bf16x8){lo[0], lo[1], lo[2], lo[3], hh[0], hh[1], hh[2], hh[3]};
;                     o[d0] = MFMA32(__builtin_bit_cast(bf16x8, P[j][ks]), vf, o[d0]);
;                 }
;             AT_LDSWAIT();
;         }
;         __builtin_amdgcn_sched_barrier(0);
;     }
.LBB0_362:
	s_andn2_b64 vcc, exec, s[54:55]
	s_cbranch_vccnz .LBB0_364
	v_lshl_add_u32 v2, v120, 3, v120
	v_lshlrev_b32_e32 v2, 10, v2
	v_cmp_lt_i32_e32 vcc, -1, v119
	s_waitcnt vmcnt(0)
	v_cvt_scalef32_pk_bf16_fp8 v86, v41, s80
	v_cvt_scalef32_pk_bf16_fp8 v87, v41, s80 op_sel:[1,0,0]
	v_cndmask_b32_e32 v2, 0, v2, vcc
	v_lshl_add_u64 v[84:85], v[112:113], 0, v[2:3]
	v_lshl_add_u32 v2, v118, 3, v118
	v_lshlrev_b32_e32 v2, 10, v2
	v_cmp_lt_i32_e32 vcc, -1, v117
	s_waitcnt lgkmcnt(1)
	global_load_dwordx4 v[100:103], v[84:85], off offset:2048
	v_cvt_pk_bf16_f32 v76, v156, v157
	v_cndmask_b32_e32 v2, 0, v2, vcc
	v_lshl_add_u64 v[84:85], v[112:113], 0, v[2:3]
	s_waitcnt lgkmcnt(0)
	global_load_dwordx4 v[104:107], v[84:85], off offset:2048
	v_cvt_scalef32_pk_bf16_fp8 v84, v40, s80
	v_cvt_scalef32_pk_bf16_fp8 v85, v40, s80 op_sel:[1,0,0]
	v_add3_u32 v2, v63, v74, v65
	ds_write_b128 v2, v[84:87]
	v_cvt_scalef32_pk_bf16_fp8 v84, v42, s80
	v_cvt_scalef32_pk_bf16_fp8 v85, v42, s80 op_sel:[1,0,0]
	v_cvt_scalef32_pk_bf16_fp8 v86, v43, s80
	v_cvt_scalef32_pk_bf16_fp8 v87, v43, s80 op_sel:[1,0,0]
	ds_write_b128 v2, v[84:87] offset:16
	v_cvt_scalef32_pk_bf16_fp8 v84, v36, s80
	v_cvt_scalef32_pk_bf16_fp8 v85, v36, s80 op_sel:[1,0,0]
	v_cvt_scalef32_pk_bf16_fp8 v86, v37, s80
	v_cvt_scalef32_pk_bf16_fp8 v87, v37, s80 op_sel:[1,0,0]
	v_add3_u32 v2, v63, v69, v65
	ds_write_b128 v2, v[84:87]
	v_cvt_scalef32_pk_bf16_fp8 v84, v38, s80
	v_cvt_scalef32_pk_bf16_fp8 v85, v38, s80 op_sel:[1,0,0]
	v_cvt_scalef32_pk_bf16_fp8 v86, v39, s80
	v_cvt_scalef32_pk_bf16_fp8 v87, v39, s80 op_sel:[1,0,0]
	ds_write_b128 v2, v[84:87] offset:16
	s_waitcnt lgkmcnt(0)
	v_cvt_pk_bf16_f32 v77, v158, v159
	v_cvt_pk_bf16_f32 v78, v160, v161
	v_cvt_pk_bf16_f32 v79, v162, v163
	ds_read_b64_tr_b16 v[84:85], v54
	ds_read_b64_tr_b16 v[86:87], v54 offset:512
	s_waitcnt lgkmcnt(0)
	v_mfma_f32_32x32x16_bf16 v[4:19], v[76:79], v[84:87], v[4:19]
	v_cvt_pk_bf16_f32 v80, v164, v165
	v_cvt_pk_bf16_f32 v81, v166, v167
	v_cvt_pk_bf16_f32 v82, v168, v169
	v_cvt_pk_bf16_f32 v83, v170, v171
	ds_read_b64_tr_b16 v[84:85], v54 offset:1024
	ds_read_b64_tr_b16 v[86:87], v54 offset:1536
	s_waitcnt lgkmcnt(0)
	v_mfma_f32_32x32x16_bf16 v[4:19], v[80:83], v[84:87], v[4:19]
	ds_read_b64_tr_b16 v[84:85], v54 offset:2048
	ds_read_b64_tr_b16 v[86:87], v54 offset:2560
	s_waitcnt lgkmcnt(0)
	v_mfma_f32_32x32x16_bf16 v[20:35], v[76:79], v[84:87], v[20:35]
	ds_read_b64_tr_b16 v[76:77], v54 offset:3072
	ds_read_b64_tr_b16 v[78:79], v54 offset:3584
	s_waitcnt lgkmcnt(0)
	s_waitcnt lgkmcnt(0)
	v_mfma_f32_32x32x16_bf16 v[20:35], v[80:83], v[76:79], v[20:35]
.LBB0_364:
	s_andn2_b64 vcc, exec, s[56:57]
	s_cbranch_vccnz .LBB0_366
	v_lshl_add_u32 v2, v149, 3, v149
	v_lshlrev_b32_e32 v2, 10, v2
	v_cmp_lt_i32_e32 vcc, -1, v148
	s_waitcnt vmcnt(0) lgkmcnt(0)
	v_cvt_scalef32_pk_bf16_fp8 v80, v104, s80
	v_cvt_scalef32_pk_bf16_fp8 v81, v104, s80 op_sel:[1,0,0]
	v_cndmask_b32_e32 v2, 0, v2, vcc
	v_lshl_add_u64 v[36:37], v[112:113], 0, v[2:3]
	v_lshl_add_u32 v2, v147, 3, v147
	v_lshlrev_b32_e32 v2, 10, v2
	v_cmp_lt_i32_e32 vcc, -1, v146
	v_cvt_scalef32_pk_bf16_fp8 v82, v105, s80
	v_cvt_scalef32_pk_bf16_fp8 v83, v105, s80 op_sel:[1,0,0]
	v_cndmask_b32_e32 v2, 0, v2, vcc
	v_lshl_add_u64 v[40:41], v[112:113], 0, v[2:3]
	global_load_dwordx4 v[36:39], v[36:37], off offset:2048
	s_nop 0
	global_load_dwordx4 v[40:43], v[40:41], off offset:2048
	v_add3_u32 v2, v63, v74, v65
	ds_write_b128 v2, v[80:83]
	v_cvt_scalef32_pk_bf16_fp8 v80, v106, s80
	v_cvt_scalef32_pk_bf16_fp8 v81, v106, s80 op_sel:[1,0,0]
	v_cvt_scalef32_pk_bf16_fp8 v82, v107, s80
	v_cvt_scalef32_pk_bf16_fp8 v83, v107, s80 op_sel:[1,0,0]
	ds_write_b128 v2, v[80:83] offset:16
	v_cvt_scalef32_pk_bf16_fp8 v80, v100, s80
	v_cvt_scalef32_pk_bf16_fp8 v81, v100, s80 op_sel:[1,0,0]
	v_cvt_scalef32_pk_bf16_fp8 v82, v101, s80
	v_cvt_scalef32_pk_bf16_fp8 v83, v101, s80 op_sel:[1,0,0]
	v_add3_u32 v2, v63, v69, v65
	ds_write_b128 v2, v[80:83]
	v_cvt_scalef32_pk_bf16_fp8 v80, v102, s80
	v_cvt_scalef32_pk_bf16_fp8 v81, v102, s80 op_sel:[1,0,0]
	v_cvt_scalef32_pk_bf16_fp8 v82, v103, s80
	v_cvt_scalef32_pk_bf16_fp8 v83, v103, s80 op_sel:[1,0,0]
	ds_write_b128 v2, v[80:83] offset:16
	s_waitcnt lgkmcnt(0)
	v_cvt_pk_bf16_f32 v76, v145, v150
	v_cvt_pk_bf16_f32 v77, v151, v152
	v_cvt_pk_bf16_f32 v78, v153, v154
	v_cvt_pk_bf16_f32 v79, v155, v75
	ds_read_b64_tr_b16 v[80:81], v54
	ds_read_b64_tr_b16 v[82:83], v54 offset:512
	v_cvt_pk_bf16_f32 v84, v70, v72
	ds_read_b64_tr_b16 v[88:89], v54 offset:1024
	ds_read_b64_tr_b16 v[90:91], v54 offset:1536
	s_waitcnt lgkmcnt(2)
	v_mfma_f32_32x32x16_bf16 v[4:19], v[76:79], v[80:83], v[4:19]
	v_cvt_pk_bf16_f32 v87, v71, v73
	ds_read_b64_tr_b16 v[70:71], v54 offset:2048
	ds_read_b64_tr_b16 v[72:73], v54 offset:2560
	ds_read_b64_tr_b16 v[80:81], v54 offset:3072
	ds_read_b64_tr_b16 v[82:83], v54 offset:3584
	v_cvt_pk_bf16_f32 v85, v64, v66
	v_cvt_pk_bf16_f32 v86, v67, v68
	s_waitcnt lgkmcnt(0)
	s_waitcnt lgkmcnt(2)
	v_mfma_f32_32x32x16_bf16 v[20:35], v[76:79], v[70:73], v[20:35]
	v_mfma_f32_32x32x16_bf16 v[4:19], v[84:87], v[88:91], v[4:19]
	s_waitcnt lgkmcnt(0)
	v_mfma_f32_32x32x16_bf16 v[20:35], v[84:87], v[80:83], v[20:35]

; #define LAS __attribute__((address_space(3)))
; __device__ __forceinline__ int crow(int r, int hi) { return (r & 3) + 8 * (r >> 2) + 4 * hi; }
; template <bool FIRST, int NB> ...
;     ...
;     if (hi == 0) { wsf[r32] = mx_true; wsf[32 + r32] = lsum; }
;     asm volatile("s_waitcnt lgkmcnt(0)" ::: "memory");
;     f32x4 mt4[4], lt4[4];
; #pragma unroll
;     for (int k = 0; k < 4; ++k) { mt4[k] = *(const LAS f32x4*)(wsf + 8 * k + 4 * hi); lt4[k] = *(const LAS f32x4*)(wsf + 32 + 8 * k + 4 * hi); }
;     if (FIRST) {
; #pragma unroll
;         for (int r = 0; r < 16; ++r) { const int q = crow(r, hi); const int trow = q * trow_mul + trow_add;
;             ACC[trow * ACCP + r32] = o[0][r]; ACC[trow * ACCP + 32 + r32] = o[1][r];
;             if (r32 == 0) { ML[trow * 2] = mt4[r >> 2][r & 3]; ML[trow * 2 + 1] = lt4[r >> 2][r & 3]; } }
.LBB0_370:
	s_or_b64 exec, exec, s[0:1]
	s_waitcnt lgkmcnt(0)
	v_lshl_add_u32 v2, v116, 2, s78
	ds_read_b128 v[64:67], v2
	ds_read_b128 v[56:59], v2 offset:32
	ds_read_b128 v[60:63], v2 offset:128
	ds_read_b128 v[52:55], v2 offset:160
	ds_read_b128 v[48:51], v2 offset:64
	s_waitcnt vmcnt(0)
	ds_read_b128 v[40:43], v2 offset:96
	ds_read_b128 v[44:47], v2 offset:192
	ds_read_b128 v[36:39], v2 offset:224
	v_add_u32_e32 v68, s27, v116
	v_lshl_add_u32 v2, v68, 4, v68
	v_lshlrev_b32_e32 v2, 4, v2
	v_add_u32_e32 v69, 0, v2
	v_cmp_ne_u32_e32 vcc, 0, v111
	v_lshl_add_u32 v2, v111, 2, v69
	ds_write2_b32 v2, v4, v20 offset1:32
	s_and_saveexec_b64 s[0:1], vcc
	s_xor_b64 s[0:1], exec, s[0:1]
	ds_write2_b32 v2, v5, v21 offset0:68 offset1:100
	s_andn2_saveexec_b64 s[0:1], s[0:1]
	s_cbranch_execz .LBB0_374
	v_lshl_add_u32 v4, v68, 3, 0
	v_add_u32_e32 v4, 0x11000, v4
	s_waitcnt lgkmcnt(8)
	v_mov_b32_e32 v70, v64
	s_waitcnt lgkmcnt(6)
	v_mov_b32_e32 v71, v60
	v_mov_b32_e32 v60, v65
	ds_write_b64 v4, v[70:71]
	ds_write2_b32 v69, v5, v21 offset0:68 offset1:100
	ds_write_b64 v4, v[60:61] offset:8

; #define LAS __attribute__((address_space(3)))
; __device__ __forceinline__ int crow(int r, int hi) { return (r & 3) + 8 * (r >> 2) + 4 * hi; }
; template <bool FIRST, int NB> ...
;     ...
;     if (hi == 0) { wsf[r32] = mx_true; wsf[32 + r32] = lsum; }
;     asm volatile("s_waitcnt lgkmcnt(0)" ::: "memory");
;     f32x4 mt4[4], lt4[4];
; #pragma unroll
;     for (int k = 0; k < 4; ++k) { mt4[k] = *(const LAS f32x4*)(wsf + 8 * k + 4 * hi); lt4[k] = *(const LAS f32x4*)(wsf + 32 + 8 * k + 4 * hi); }
;     if (FIRST) {
; #pragma unroll
;         for (int r = 0; r < 16; ++r) { const int q = crow(r, hi); const int trow = q * trow_mul + trow_add;
;             ACC[trow * ACCP + r32] = o[0][r]; ACC[trow * ACCP + 32 + r32] = o[1][r];
;             if (r32 == 0) { ML[trow * 2] = mt4[r >> 2][r & 3]; ML[trow * 2 + 1] = lt4[r >> 2][r & 3]; } }
;     } else {
;         f32x2 ml[16]; float a0[16], a1[16];
; #pragma unroll
;         for (int r = 0; r < 16; ++r) { const int q = crow(r, hi); const int trow = q * trow_mul + trow_add;
;             ml[r] = *(const LAS f32x2*)(ML + trow * 2); a0[r] = ACC[trow * ACCP + r32]; a1[r] = ACC[trow * ACCP + 32 + r32]; }
;         asm volatile("s_waitcnt lgkmcnt(0)" ::: "memory");
; #pragma unroll
;         for (int r = 0; r < 16; ++r) { const int q = crow(r, hi); const int trow = q * trow_mul + trow_add;
;             const float mt = mt4[r >> 2][r & 3], lt = lt4[r >> 2][r & 3], mo = ml[r][0], lo_ = ml[r][1];
;             const float mn = fmaxf(mo, mt); const float fa = __builtin_amdgcn_exp2f(mo - mn), fb = __builtin_amdgcn_exp2f(mt - mn);
;             ACC[trow * ACCP + r32] = a0[r] * fa + o[0][r] * fb; ACC[trow * ACCP + 32 + r32] = a1[r] * fa + o[1][r] * fb;
;             if (r32 == 0) { ML[trow * 2] = mn; ML[trow * 2 + 1] = lo_ * fa + lt * fb; } }
.LBB0_461:
	s_or_b64 exec, exec, s[0:1]
	s_waitcnt lgkmcnt(0)
	v_lshl_add_u32 v2, v111, 2, s78
	ds_read_b128 v[66:69], v2
	ds_read_b128 v[58:61], v2 offset:32
	ds_read_b128 v[62:65], v2 offset:128
	ds_read_b128 v[54:57], v2 offset:160
	ds_read_b128 v[50:53], v2 offset:64
	ds_read_b128 v[12:15], v2 offset:192
	ds_read_b128 v[8:11], v2 offset:96
	ds_read_b128 v[4:7], v2 offset:224
	v_lshlrev_b32_e32 v2, 1, v111
	v_add_u32_e32 v16, s25, v2
	v_lshlrev_b32_e32 v133, 3, v16
	v_lshl_add_u32 v16, v16, 4, v16
	v_lshlrev_b32_e32 v16, 4, v16
	v_lshlrev_b32_e32 v72, 2, v132
	v_readlane_b32 s0, v255, 11
	v_add3_u32 v174, 0, v16, v72
	v_add_u32_e32 v17, s96, v133
	v_add_u32_e32 v16, s0, v2
	v_lshlrev_b32_e32 v170, 3, v16
	v_lshl_add_u32 v16, v16, 4, v16
	v_lshlrev_b32_e32 v16, 4, v16
	v_readlane_b32 s0, v255, 12
	v_add3_u32 v171, 0, v16, v72
	ds_read_b64 v[130:131], v17
	v_add_u32_e32 v16, s0, v2
	v_add_u32_e32 v17, s96, v170
	v_lshlrev_b32_e32 v167, 3, v16
	v_lshl_add_u32 v16, v16, 4, v16
	v_lshlrev_b32_e32 v16, 4, v16
	ds_read_b64 v[126:127], v17
	v_add_u32_e32 v17, s96, v167
	v_add3_u32 v169, 0, v16, v72
	v_lshl_or_b32 v16, v110, 1, 6
	ds_read_b64 v[120:121], v17
	v_add_u32_e32 v17, s25, v16
	v_lshlrev_b32_e32 v166, 3, v17
	v_lshl_add_u32 v17, v17, 4, v17
	v_lshlrev_b32_e32 v17, 4, v17
	v_add3_u32 v168, 0, v17, v72
	v_add_u32_e32 v17, s79, v2
	v_lshlrev_b32_e32 v164, 3, v17
	v_lshl_add_u32 v17, v17, 4, v17
	v_lshlrev_b32_e32 v17, 4, v17
	v_readlane_b32 s0, v255, 13
	v_add3_u32 v165, 0, v17, v72
	v_add_u32_e32 v70, s96, v166
	v_add_u32_e32 v17, s0, v2
	v_lshlrev_b32_e32 v162, 3, v17
	v_lshl_add_u32 v17, v17, 4, v17
	v_lshlrev_b32_e32 v17, 4, v17
	v_readlane_b32 s0, v255, 14
	v_add3_u32 v163, 0, v17, v72
	ds_read_b64 v[118:119], v70
	v_add_u32_e32 v17, s0, v2
	v_lshlrev_b32_e32 v160, 3, v17
	v_lshl_add_u32 v17, v17, 4, v17
	v_lshlrev_b32_e32 v17, 4, v17
	v_add3_u32 v161, 0, v17, v72
	v_add_u32_e32 v17, s79, v16
	v_lshlrev_b32_e32 v158, 3, v17
	v_lshl_add_u32 v17, v17, 4, v17
	v_lshlrev_b32_e32 v17, 4, v17
	v_add3_u32 v159, 0, v17, v72
	v_add_u32_e32 v17, s83, v2
	v_lshlrev_b32_e32 v156, 3, v17
	v_lshl_add_u32 v17, v17, 4, v17
	v_lshlrev_b32_e32 v17, 4, v17
	v_readlane_b32 s0, v255, 15
	v_add3_u32 v157, 0, v17, v72
	v_add_u32_e32 v70, s96, v164
	v_add_u32_e32 v17, s0, v2
	v_lshlrev_b32_e32 v154, 3, v17
	v_lshl_add_u32 v17, v17, 4, v17
	v_lshlrev_b32_e32 v17, 4, v17
	v_readlane_b32 s0, v255, 16
	v_add3_u32 v155, 0, v17, v72
	ds_read_b64 v[114:115], v70
	v_add_u32_e32 v17, s0, v2
	v_lshlrev_b32_e32 v152, 3, v17
	v_lshl_add_u32 v17, v17, 4, v17
	v_lshlrev_b32_e32 v17, 4, v17
	v_add_u32_e32 v70, s96, v162
	v_add3_u32 v153, 0, v17, v72
	v_add_u32_e32 v17, s83, v16
	ds_read_b64 v[110:111], v70
	v_add_u32_e32 v70, s96, v160
	v_lshlrev_b32_e32 v150, 3, v17
	v_lshl_add_u32 v17, v17, 4, v17
	v_lshlrev_b32_e32 v17, 4, v17
	ds_read_b64 v[102:103], v70
	v_add_u32_e32 v70, s96, v158
	v_add3_u32 v151, 0, v17, v72
	v_add_u32_e32 v17, s29, v2
	ds_read_b64 v[100:101], v70
	v_add_u32_e32 v70, s96, v156
	v_lshlrev_b32_e32 v148, 3, v17
	v_lshl_add_u32 v17, v17, 4, v17
	v_lshlrev_b32_e32 v17, 4, v17
	v_readlane_b32 s0, v255, 17
	s_waitcnt vmcnt(0)
	ds_read_b64 v[96:97], v70
	v_add_u32_e32 v70, s96, v154
	v_add3_u32 v149, 0, v17, v72
	v_add_u32_e32 v17, s0, v2
	v_readlane_b32 s0, v255, 18
	ds_read_b64 v[92:93], v70
	v_add_u32_e32 v70, s96, v152
	v_add_u32_e32 v2, s0, v2
	v_cmp_eq_u32_e32 vcc, 0, v132
	s_waitcnt lgkmcnt(14)
	v_max_f32_e32 v132, v66, v66
	s_waitcnt lgkmcnt(9)
	v_max_f32_e32 v175, v130, v130
	ds_read_b64 v[86:87], v70
	v_add_u32_e32 v70, s96, v150
	v_lshlrev_b32_e32 v144, 3, v2
	v_lshl_add_u32 v2, v2, 4, v2
	v_lshlrev_b32_e32 v2, 4, v2
	v_add_u32_e32 v73, s29, v16
	v_max_f32_e32 v132, v175, v132
	ds_read_b64 v[84:85], v70
	v_add_u32_e32 v70, s96, v148
	v_lshlrev_b32_e32 v146, 3, v17
	v_lshl_add_u32 v17, v17, 4, v17
	v_lshlrev_b32_e32 v17, 4, v17
	v_add3_u32 v145, 0, v2, v72
	v_lshlrev_b32_e32 v2, 3, v73
	v_lshl_add_u32 v73, v73, 4, v73
	v_lshlrev_b32_e32 v73, 4, v73
	v_sub_f32_e32 v66, v66, v132
	ds_read2_b32 v[172:173], v174 offset1:32
	ds_read_b64 v[80:81], v70
	v_add_u32_e32 v70, s96, v146
	v_add3_u32 v147, 0, v17, v72
	v_add_u32_e32 v17, s96, v144
	v_add_u32_e32 v16, s96, v2
	v_add3_u32 v143, 0, v73, v72
	v_sub_f32_e32 v130, v130, v132
	v_exp_f32_e32 v66, v66
	ds_read2_b32 v[128:129], v171 offset1:32
	ds_read2_b32 v[124:125], v169 offset1:32
	ds_read2_b32 v[122:123], v168 offset1:32
	ds_read2_b32 v[116:117], v165 offset1:32
	ds_read2_b32 v[112:113], v163 offset1:32
	ds_read2_b32 v[106:107], v161 offset1:32
	ds_read2_b32 v[104:105], v159 offset1:32
	ds_read2_b32 v[98:99], v157 offset1:32
	ds_read2_b32 v[94:95], v155 offset1:32
	ds_read2_b32 v[90:91], v153 offset1:32
	ds_read2_b32 v[88:89], v151 offset1:32
	ds_read2_b32 v[82:83], v149 offset1:32
	ds_read_b64 v[76:77], v70
	ds_read2_b32 v[78:79], v147 offset1:32
	ds_read_b64 v[70:71], v17
	ds_read2_b32 v[74:75], v145 offset1:32
	ds_read_b64 v[16:17], v16
	ds_read2_b32 v[72:73], v143 offset1:32
	v_exp_f32_e32 v130, v130
	s_waitcnt lgkmcnt(0)
	v_mul_f32_e32 v18, v18, v66
	v_mul_f32_e32 v34, v34, v66
	s_waitcnt lgkmcnt(14)
; __device__ __forceinline__ int crow(int r, int hi) { return (r & 3) + 8 * (r >> 2) + 4 * hi; }
; template <bool FIRST, int NB> ...
;     ...
; #pragma unroll
;         for (int r = 0; r < 16; ++r) { const int q = crow(r, hi); const int trow = q * trow_mul + trow_add;
;             const float mt = mt4[r >> 2][r & 3], lt = lt4[r >> 2][r & 3], mo = ml[r][0], lo_ = ml[r][1];
;             const float mn = fmaxf(mo, mt); const float fa = __builtin_amdgcn_exp2f(mo - mn), fb = __builtin_amdgcn_exp2f(mt - mn);
;             ACC[trow * ACCP + r32] = a0[r] * fa + o[0][r] * fb; ACC[trow * ACCP + 32 + r32] = a1[r] * fa + o[1][r] * fb;
;             if (r32 == 0) { ML[trow * 2] = mn; ML[trow * 2 + 1] = lo_ * fa + lt * fb; } }
	v_fmac_f32_e32 v18, v172, v130
	v_fmac_f32_e32 v34, v173, v130
	ds_write2_b32 v174, v18, v34 offset1:32
	s_and_saveexec_b64 s[0:1], vcc
	v_add_u32_e32 v18, 0, v133
	v_mul_f32_e32 v133, v62, v66
	v_add_u32_e32 v18, 0x11000, v18
	v_fmac_f32_e32 v133, v131, v130
	ds_write_b64 v18, v[132:133]
	s_or_b64 exec, exec, s[0:1]
	v_max_f32_e32 v18, v67, v67
	v_max_f32_e32 v34, v126, v126
	v_max_f32_e32 v18, v34, v18
	v_sub_f32_e32 v62, v67, v18
	v_sub_f32_e32 v34, v126, v18
	v_exp_f32_e32 v62, v62
	v_exp_f32_e32 v34, v34
	v_mul_f32_e32 v19, v19, v62
	v_mul_f32_e32 v35, v35, v62
	v_fmac_f32_e32 v19, v128, v34
	v_fmac_f32_e32 v35, v129, v34
	ds_write2_b32 v171, v19, v35 offset1:32
	s_and_saveexec_b64 s[0:1], vcc
	v_add_u32_e32 v19, 0, v170
	v_add_u32_e32 v35, 0x11000, v19
	v_mul_f32_e32 v19, v63, v62
	v_fmac_f32_e32 v19, v127, v34
	ds_write_b64 v35, v[18:19]
	s_or_b64 exec, exec, s[0:1]
	v_max_f32_e32 v18, v68, v68
	v_max_f32_e32 v19, v120, v120
	v_max_f32_e32 v18, v19, v18
	v_sub_f32_e32 v19, v68, v18
	v_sub_f32_e32 v34, v120, v18
	v_exp_f32_e32 v19, v19
	v_exp_f32_e32 v34, v34
	v_mul_f32_e32 v20, v20, v19
	v_mul_f32_e32 v35, v36, v19
	v_fmac_f32_e32 v20, v124, v34
	v_fmac_f32_e32 v35, v125, v34
	ds_write2_b32 v169, v20, v35 offset1:32
	s_and_saveexec_b64 s[0:1], vcc
	v_add_u32_e32 v20, 0, v167
	v_mul_f32_e32 v19, v64, v19
	v_add_u32_e32 v20, 0x11000, v20
	v_fmac_f32_e32 v19, v121, v34
	ds_write_b64 v20, v[18:19]
	s_or_b64 exec, exec, s[0:1]
	v_max_f32_e32 v18, v69, v69
	v_max_f32_e32 v19, v118, v118
	v_max_f32_e32 v18, v19, v18
	v_sub_f32_e32 v19, v69, v18
	v_sub_f32_e32 v20, v118, v18
	v_exp_f32_e32 v19, v19
	v_exp_f32_e32 v20, v20
	v_mul_f32_e32 v21, v21, v19
	v_mul_f32_e32 v34, v37, v19
	v_fmac_f32_e32 v21, v122, v20
	v_fmac_f32_e32 v34, v123, v20
	ds_write2_b32 v168, v21, v34 offset1:32
	s_and_saveexec_b64 s[0:1], vcc
	v_add_u32_e32 v21, 0, v166
	v_mul_f32_e32 v19, v65, v19
	v_add_u32_e32 v21, 0x11000, v21
	v_fmac_f32_e32 v19, v119, v20
	ds_write_b64 v21, v[18:19]
	s_or_b64 exec, exec, s[0:1]
	v_max_f32_e32 v18, v58, v58
	v_max_f32_e32 v19, v114, v114
	v_max_f32_e32 v18, v19, v18
	v_sub_f32_e32 v19, v58, v18
	v_sub_f32_e32 v20, v114, v18
	v_exp_f32_e32 v19, v19
	v_exp_f32_e32 v20, v20
	v_mul_f32_e32 v21, v22, v19
	v_mul_f32_e32 v22, v38, v19
	v_fmac_f32_e32 v21, v116, v20
	v_fmac_f32_e32 v22, v117, v20
	ds_write2_b32 v165, v21, v22 offset1:32
	s_and_saveexec_b64 s[0:1], vcc
	v_add_u32_e32 v21, 0, v164
	v_mul_f32_e32 v19, v54, v19
	v_add_u32_e32 v21, 0x11000, v21
	v_fmac_f32_e32 v19, v115, v20
	ds_write_b64 v21, v[18:19]
	s_or_b64 exec, exec, s[0:1]
	v_max_f32_e32 v18, v59, v59
	v_max_f32_e32 v19, v110, v110
	v_max_f32_e32 v18, v19, v18
	v_sub_f32_e32 v19, v59, v18
	v_sub_f32_e32 v20, v110, v18
	v_exp_f32_e32 v19, v19
	v_exp_f32_e32 v20, v20
	v_mul_f32_e32 v21, v23, v19
	v_mul_f32_e32 v22, v39, v19
	s_waitcnt lgkmcnt(14)
	v_fmac_f32_e32 v21, v112, v20
	v_fmac_f32_e32 v22, v113, v20
	ds_write2_b32 v163, v21, v22 offset1:32
	s_and_saveexec_b64 s[0:1], vcc
	v_add_u32_e32 v21, 0, v162
	v_mul_f32_e32 v19, v55, v19
	v_add_u32_e32 v21, 0x11000, v21
	v_fmac_f32_e32 v19, v111, v20
	ds_write_b64 v21, v[18:19]
	s_or_b64 exec, exec, s[0:1]
	v_max_f32_e32 v18, v60, v60
	v_max_f32_e32 v19, v102, v102
	v_max_f32_e32 v18, v19, v18
	v_sub_f32_e32 v19, v60, v18
	v_sub_f32_e32 v20, v102, v18
	v_exp_f32_e32 v19, v19
	v_exp_f32_e32 v20, v20
	v_mul_f32_e32 v21, v24, v19
	v_mul_f32_e32 v22, v40, v19
	v_fmac_f32_e32 v21, v106, v20
	v_fmac_f32_e32 v22, v107, v20
	ds_write2_b32 v161, v21, v22 offset1:32
	s_and_saveexec_b64 s[0:1], vcc
	v_add_u32_e32 v21, 0, v160
	v_mul_f32_e32 v19, v56, v19
	v_add_u32_e32 v21, 0x11000, v21
	v_fmac_f32_e32 v19, v103, v20
	ds_write_b64 v21, v[18:19]
	s_or_b64 exec, exec, s[0:1]
	v_max_f32_e32 v18, v61, v61
	v_max_f32_e32 v19, v100, v100
	v_max_f32_e32 v18, v19, v18
	v_sub_f32_e32 v19, v61, v18
	v_sub_f32_e32 v20, v100, v18
	v_exp_f32_e32 v19, v19
	v_exp_f32_e32 v20, v20
	v_mul_f32_e32 v21, v25, v19
	v_mul_f32_e32 v22, v41, v19
	v_fmac_f32_e32 v21, v104, v20
	v_fmac_f32_e32 v22, v105, v20
	ds_write2_b32 v159, v21, v22 offset1:32
	s_and_saveexec_b64 s[0:1], vcc
	v_add_u32_e32 v21, 0, v158
	v_mul_f32_e32 v19, v57, v19
	v_add_u32_e32 v21, 0x11000, v21
	v_fmac_f32_e32 v19, v101, v20
	ds_write_b64 v21, v[18:19]
	s_or_b64 exec, exec, s[0:1]
	v_max_f32_e32 v18, v50, v50
	v_max_f32_e32 v19, v96, v96
	v_max_f32_e32 v18, v19, v18
	v_sub_f32_e32 v19, v50, v18
	v_sub_f32_e32 v20, v96, v18
	v_exp_f32_e32 v19, v19
	v_exp_f32_e32 v20, v20
	v_mul_f32_e32 v21, v26, v19
	v_mul_f32_e32 v22, v42, v19
	v_fmac_f32_e32 v21, v98, v20
	v_fmac_f32_e32 v22, v99, v20
	ds_write2_b32 v157, v21, v22 offset1:32
	s_and_saveexec_b64 s[0:1], vcc
	v_add_u32_e32 v21, 0, v156
	v_mul_f32_e32 v19, v12, v19
	v_add_u32_e32 v21, 0x11000, v21
	v_fmac_f32_e32 v19, v97, v20
	ds_write_b64 v21, v[18:19]
	s_or_b64 exec, exec, s[0:1]
	v_max_f32_e32 v12, v51, v51
	v_max_f32_e32 v18, v92, v92
	v_max_f32_e32 v12, v18, v12
	v_sub_f32_e32 v19, v51, v12
	v_sub_f32_e32 v18, v92, v12
	v_exp_f32_e32 v19, v19
	v_exp_f32_e32 v18, v18
	v_mul_f32_e32 v20, v27, v19
	v_mul_f32_e32 v21, v43, v19
	v_fmac_f32_e32 v20, v94, v18
	v_fmac_f32_e32 v21, v95, v18
	ds_write2_b32 v155, v20, v21 offset1:32
	s_and_saveexec_b64 s[0:1], vcc
	v_add_u32_e32 v20, 0, v154
	v_mul_f32_e32 v13, v13, v19
	v_add_u32_e32 v20, 0x11000, v20
	v_fmac_f32_e32 v13, v93, v18
	ds_write_b64 v20, v[12:13]
	s_or_b64 exec, exec, s[0:1]
	v_max_f32_e32 v12, v52, v52
	v_max_f32_e32 v13, v86, v86
	v_max_f32_e32 v12, v13, v12
	v_sub_f32_e32 v13, v52, v12
	v_sub_f32_e32 v18, v86, v12
	v_exp_f32_e32 v13, v13
	v_exp_f32_e32 v18, v18
	v_mul_f32_e32 v19, v28, v13
	v_mul_f32_e32 v20, v44, v13
	s_waitcnt lgkmcnt(14)
; #define LAS __attribute__((address_space(3)))
; __device__ __forceinline__ int crow(int r, int hi) { return (r & 3) + 8 * (r >> 2) + 4 * hi; }
; #define AT_LOADROWS(dst, l0, ls, col) do { _Pragma("unroll") for (int i_ = 0; i_ < 2; ++i_) { int l_ = (l0) + (ls) * (16 * i_ + lr); l_ = l_ < 0 ? 0 : (l_ > L - 1 ? L - 1 : l_); \
;         dst[i_] = *(const GAS u32x4*)(base + (size_t)l_ * rstride + (col)); } } while (0)
; template <bool FIRST, int NB> ...
;     asm volatile("" : "+v"(lane));
;     const int r32 = lane & 31, hi = lane >> 5, lr = lane >> 2, lc = lane & 3;
;     const int qcol = ((g * 3 + 0) * 16 + h) * 64, kcol = ((g * 3 + 1) * 16 + h) * 64, vcol = ((g * 3 + 2) * 16 + h) * 64;
;     const size_t rstride = (size_t)dil * NQKV;
;     const unsigned char* base = QKVb + (size_t)cls * NQKV + lc * 16;
;     const int jlo = (kb0 >= -31) ? 0 : ((-kb0) >> 5);
;     const int qpos = q0 + QS * r32;
;     const int dmax = qpos < 128 ? qpos : 128;
;     const float half = 0.5f * (float)dmax;
;     ...
;     u32x4 kr[2][2];
;     i32x8 qf8;
;     { u32x4 qr[2]; AT_LOADROWS(qr, q0, QS, qcol);
; #pragma unroll
;       for (int j = 0; j < NB; ++j) if (j == jlo) AT_LOADROWS(kr[j & 1], kb0 + 32 * j, 1, kcol);
;     ...
; #pragma unroll
;         for (int r = 0; r < 16; ++r) { const int q = crow(r, hi); const int trow = q * trow_mul + trow_add;
;             const float mt = mt4[r >> 2][r & 3], lt = lt4[r >> 2][r & 3], mo = ml[r][0], lo_ = ml[r][1];
;             const float mn = fmaxf(mo, mt); const float fa = __builtin_amdgcn_exp2f(mo - mn), fb = __builtin_amdgcn_exp2f(mt - mn);
;             ACC[trow * ACCP + r32] = a0[r] * fa + o[0][r] * fb; ACC[trow * ACCP + 32 + r32] = a1[r] * fa + o[1][r] * fb;
;             if (r32 == 0) { ML[trow * 2] = mn; ML[trow * 2 + 1] = lo_ * fa + lt * fb; } }
	v_fmac_f32_e32 v19, v90, v18
	v_fmac_f32_e32 v20, v91, v18
	ds_write2_b32 v153, v19, v20 offset1:32
	s_and_saveexec_b64 s[0:1], vcc
	v_add_u32_e32 v19, 0, v152
	v_mul_f32_e32 v13, v14, v13
	v_add_u32_e32 v19, 0x11000, v19
	v_fmac_f32_e32 v13, v87, v18
	ds_write_b64 v19, v[12:13]
	s_or_b64 exec, exec, s[0:1]
	v_max_f32_e32 v12, v53, v53
	v_max_f32_e32 v13, v84, v84
	v_max_f32_e32 v12, v13, v12
	v_sub_f32_e32 v13, v53, v12
	v_sub_f32_e32 v14, v84, v12
	v_exp_f32_e32 v13, v13
	v_exp_f32_e32 v14, v14
	v_mul_f32_e32 v18, v29, v13
	v_mul_f32_e32 v19, v45, v13
	v_fmac_f32_e32 v18, v88, v14
	v_fmac_f32_e32 v19, v89, v14
	ds_write2_b32 v151, v18, v19 offset1:32
	s_and_saveexec_b64 s[0:1], vcc
	v_add_u32_e32 v18, 0, v150
	v_mul_f32_e32 v13, v15, v13
	v_add_u32_e32 v18, 0x11000, v18
	v_fmac_f32_e32 v13, v85, v14
	ds_write_b64 v18, v[12:13]
	s_or_b64 exec, exec, s[0:1]
	v_max_f32_e32 v12, v8, v8
	v_max_f32_e32 v13, v80, v80
	v_max_f32_e32 v12, v13, v12
	v_sub_f32_e32 v8, v8, v12
	v_sub_f32_e32 v14, v80, v12
	v_exp_f32_e32 v13, v8
	v_exp_f32_e32 v8, v14
	v_mul_f32_e32 v14, v30, v13
	v_mul_f32_e32 v15, v46, v13
	v_fmac_f32_e32 v14, v82, v8
	v_fmac_f32_e32 v15, v83, v8
	ds_write2_b32 v149, v14, v15 offset1:32
	s_and_saveexec_b64 s[0:1], vcc
	v_add_u32_e32 v14, 0, v148
	v_mul_f32_e32 v13, v4, v13
	v_add_u32_e32 v14, 0x11000, v14
	v_fmac_f32_e32 v13, v81, v8
	ds_write_b64 v14, v[12:13]
	s_or_b64 exec, exec, s[0:1]
	v_max_f32_e32 v4, v9, v9
	v_max_f32_e32 v8, v76, v76
	v_max_f32_e32 v4, v8, v4
	v_sub_f32_e32 v9, v9, v4
	v_sub_f32_e32 v8, v76, v4
	v_exp_f32_e32 v9, v9
	v_exp_f32_e32 v8, v8
	v_mul_f32_e32 v12, v31, v9
	v_mul_f32_e32 v13, v47, v9
	v_fmac_f32_e32 v12, v78, v8
	v_fmac_f32_e32 v13, v79, v8
	ds_write2_b32 v147, v12, v13 offset1:32
	s_and_saveexec_b64 s[0:1], vcc
	v_add_u32_e32 v12, 0, v146
	v_mul_f32_e32 v5, v5, v9
	v_add_u32_e32 v12, 0x11000, v12
	v_fmac_f32_e32 v5, v77, v8
	ds_write_b64 v12, v[4:5]
	s_or_b64 exec, exec, s[0:1]
	v_max_f32_e32 v4, v10, v10
	s_waitcnt lgkmcnt(14)
	v_max_f32_e32 v5, v70, v70
	v_max_f32_e32 v4, v5, v4
	v_sub_f32_e32 v5, v10, v4
	v_sub_f32_e32 v8, v70, v4
	v_exp_f32_e32 v5, v5
	v_exp_f32_e32 v8, v8
	v_mul_f32_e32 v9, v32, v5
	v_mul_f32_e32 v10, v48, v5
	v_fmac_f32_e32 v9, v74, v8
	v_fmac_f32_e32 v10, v75, v8
	ds_write2_b32 v145, v9, v10 offset1:32
	s_and_saveexec_b64 s[0:1], vcc
	v_add_u32_e32 v9, 0, v144
	v_mul_f32_e32 v5, v6, v5
	v_add_u32_e32 v9, 0x11000, v9
	v_fmac_f32_e32 v5, v71, v8
	ds_write_b64 v9, v[4:5]
	s_or_b64 exec, exec, s[0:1]
	v_max_f32_e32 v4, v11, v11
	v_max_f32_e32 v5, v16, v16
	v_max_f32_e32 v4, v5, v4
	v_sub_f32_e32 v5, v11, v4
	v_sub_f32_e32 v6, v16, v4
	v_exp_f32_e32 v5, v5
	v_exp_f32_e32 v6, v6
	v_mul_f32_e32 v8, v33, v5
	v_mul_f32_e32 v9, v49, v5
	v_fmac_f32_e32 v8, v72, v6
	v_fmac_f32_e32 v9, v73, v6
	ds_write2_b32 v143, v8, v9 offset1:32
	s_and_saveexec_b64 s[0:1], vcc
	v_add_u32_e32 v2, 0, v2
	v_mul_f32_e32 v5, v7, v5
	v_add_u32_e32 v2, 0x11000, v2
	v_fmac_f32_e32 v5, v17, v6
	ds_write_b64 v2, v[4:5]
	s_or_b64 exec, exec, s[0:1]
	v_readlane_b32 s0, v255, 19
	s_or_b32 s0, s6, s0
	s_lshl_b32 s2, s38, 5
	s_or_b32 s3, s2, 0xffffff80
	v_mov_b32_e32 v101, v1
	s_mul_hi_i32 s1, s0, 0x2400
	s_mulk_i32 s0, 0x2400
	s_waitcnt lgkmcnt(0)
	s_waitcnt lgkmcnt(0)
	s_barrier
	s_add_u32 s0, s40, s0
	v_and_b32_e32 v118, 3, v101
	v_ashrrev_i32_e32 v117, 2, v101
	s_addc_u32 s1, s41, s1
	v_lshlrev_b32_e32 v2, 4, v118
	v_lshl_add_u64 v[4:5], s[0:1], 0, v[2:3]
	v_add_u32_e32 v8, s2, v117
	v_mov_b32_e32 v6, 0x7f
	v_mov_b32_e32 v9, 0x6f
	v_lshl_add_u64 v[84:85], v[4:5], 0, s[22:23]
	s_mov_b64 s[0:1], 0x1800
	v_med3_i32 v6, v8, 0, v6
	v_med3_i32 v8, v8, -16, v9
	v_lshl_add_u64 v[4:5], v[84:85], 0, s[0:1]
	v_mul_u32_u24_e32 v6, 0x24000, v6
	v_mov_b32_e32 v7, v3
	v_add_u32_e32 v8, 16, v8
	v_lshl_add_u64 v[6:7], v[4:5], 0, v[6:7]
	v_mad_u64_u32 v[8:9], s[0:1], v8, s26, v[4:5]
	global_load_dwordx4 v[4:7], v[6:7], off
	s_nop 0
	global_load_dwordx4 v[8:11], v[8:9], off
	s_cmp_eq_u32 s38, 3
	v_add_u32_e32 v12, s3, v117
	s_mov_b64 s[0:1], 0x1c00
	s_cselect_b64 s[72:73], -1, 0
	s_cmp_lg_u32 s38, 3
	s_movk_i32 s9, 0xffe0
	v_mov_b32_e32 v13, 0x5f
	v_lshl_add_u64 v[44:45], v[84:85], 0, s[0:1]
	s_cselect_b64 s[0:1], -1, 0
	v_med3_i32 v87, v12, s9, v13
	s_movk_i32 s9, 0xffd0
	v_mov_b32_e32 v13, 0x4f
	s_and_b64 vcc, exec, s[0:1]
	v_med3_i32 v86, v12, s9, v13
	s_cbranch_vccnz .LBB0_495
	v_add_u32_e32 v13, 32, v87
	s_mov_b32 s9, 0x24000
	v_mad_u64_u32 v[14:15], s[10:11], v13, s9, v[44:45]
	v_add_u32_e32 v13, 48, v86
	v_mad_u64_u32 v[16:17], s[10:11], v13, s9, v[44:45]
	global_load_dwordx4 v[36:39], v[14:15], off
	global_load_dwordx4 v[40:43], v[16:17], off
	s_mov_b32 s26, 0x24000

; #define LAS __attribute__((address_space(3)))
; __device__ __forceinline__ int crow(int r, int hi) { return (r & 3) + 8 * (r >> 2) + 4 * hi; }
; template <bool FIRST, int NB> ...
;     ...
;         f32x2 ml[16]; float a0[16], a1[16];
; #pragma unroll
;         for (int r = 0; r < 16; ++r) { const int q = crow(r, hi); const int trow = q * trow_mul + trow_add;
;             ml[r] = *(const LAS f32x2*)(ML + trow * 2); a0[r] = ACC[trow * ACCP + r32]; a1[r] = ACC[trow * ACCP + 32 + r32]; }
;         asm volatile("s_waitcnt lgkmcnt(0)" ::: "memory");
; #pragma unroll
;         for (int r = 0; r < 16; ++r) { const int q = crow(r, hi); const int trow = q * trow_mul + trow_add;
;             const float mt = mt4[r >> 2][r & 3], lt = lt4[r >> 2][r & 3], mo = ml[r][0], lo_ = ml[r][1];
;             const float mn = fmaxf(mo, mt); const float fa = __builtin_amdgcn_exp2f(mo - mn), fb = __builtin_amdgcn_exp2f(mt - mn);
;             ACC[trow * ACCP + r32] = a0[r] * fa + o[0][r] * fb; ACC[trow * ACCP + 32 + r32] = a1[r] * fa + o[1][r] * fb;
;             if (r32 == 0) { ML[trow * 2] = mn; ML[trow * 2 + 1] = lo_ * fa + lt * fb; } }
.LBB0_533:
	s_or_b64 exec, exec, s[0:1]
	s_waitcnt lgkmcnt(0)
	v_lshl_add_u32 v2, v107, 2, s78
	v_lshlrev_b32_e32 v68, 3, v107
	ds_read_b128 v[64:67], v2
	ds_read_b128 v[56:59], v2 offset:32
	ds_read_b128 v[60:63], v2 offset:128
	ds_read_b128 v[52:55], v2 offset:160
	ds_read_b128 v[48:51], v2 offset:64
	ds_read_b128 v[44:47], v2 offset:192
	ds_read_b128 v[40:43], v2 offset:96
	ds_read_b128 v[36:39], v2 offset:224
	v_add_u32_e32 v2, s51, v68
	v_lshlrev_b32_e32 v133, 3, v2
	v_add_u32_e32 v69, s96, v133
	v_lshl_add_u32 v2, v2, 4, v2
	v_lshlrev_b32_e32 v2, 4, v2
	v_lshlrev_b32_e32 v72, 2, v132
	v_add_u32_e32 v164, 64, v133
	ds_read_b64 v[130:131], v69
	v_add3_u32 v2, 0, v2, v72
	v_add_u32_e32 v69, s96, v164
	ds_read_b64 v[126:127], v69
	v_add_u32_e32 v69, 0x800, v2
	v_add_u32_e32 v163, 0x80, v133
	ds_read2_b32 v[128:129], v69 offset0:32 offset1:64
	v_add_u32_e32 v69, s96, v163
	ds_read_b64 v[120:121], v69
	v_add_u32_e32 v69, 0x1000, v2
	ds_read2_b32 v[124:125], v69 offset0:64 offset1:96
	v_or_b32_e32 v69, 24, v106
	v_add_u32_e32 v70, s51, v69
	v_lshlrev_b32_e32 v161, 3, v70
	v_lshl_add_u32 v70, v70, 4, v70
	v_lshlrev_b32_e32 v70, 4, v70
	v_add3_u32 v162, 0, v70, v72
	v_add_u32_e32 v70, s28, v68
	v_lshlrev_b32_e32 v159, 3, v70
	v_lshl_add_u32 v70, v70, 4, v70
	v_lshlrev_b32_e32 v70, 4, v70
	v_add_u32_e32 v158, 0x240, v133
	v_add_u32_e32 v71, s96, v161
	v_add3_u32 v160, 0, v70, v72
	v_add_u32_e32 v70, s96, v158
	ds_read_b64 v[118:119], v71
	ds_read_b64 v[110:111], v70
	v_add_u32_e32 v70, 0x4c00, v2
	v_add_u32_e32 v157, 0x280, v133
	v_add_u32_e32 v71, s96, v159
	ds_read2_b32 v[112:113], v70 offset0:32 offset1:64
	v_add_u32_e32 v70, s96, v157
	ds_read_b64 v[114:115], v71
	ds_read_b64 v[102:103], v70
	v_add_u32_e32 v70, 0x5400, v2
	ds_read2_b32 v[106:107], v70 offset0:64 offset1:96
	v_add_u32_e32 v70, s28, v69
	v_lshlrev_b32_e32 v155, 3, v70
	v_lshl_add_u32 v70, v70, 4, v70
	v_lshlrev_b32_e32 v70, 4, v70
	v_add3_u32 v156, 0, v70, v72
	v_add_u32_e32 v70, s82, v68
	v_add_u32_e32 v68, s76, v68
	v_lshlrev_b32_e32 v153, 3, v70
	v_lshl_add_u32 v70, v70, 4, v70
	v_lshlrev_b32_e32 v70, 4, v70
	v_add_u32_e32 v152, 0x440, v133
	v_lshlrev_b32_e32 v147, 3, v68
	v_lshl_add_u32 v68, v68, 4, v68
	v_lshlrev_b32_e32 v68, 4, v68
	v_add_u32_e32 v146, 0x640, v133
	v_add_u32_e32 v71, s96, v155
	v_add3_u32 v154, 0, v70, v72
	v_add_u32_e32 v70, s96, v152
	v_add3_u32 v148, 0, v68, v72
	v_add_u32_e32 v68, s96, v146
	ds_read_b64 v[100:101], v71
	ds_read_b64 v[92:93], v70
	ds_read_b64 v[76:77], v68
	v_add_u32_e32 v70, 0x9000, v2
	v_add_u32_e32 v151, 0x480, v133
	v_add_u32_e32 v71, s96, v153
	ds_read2_b32 v[94:95], v70 offset0:32 offset1:64
	v_add_u32_e32 v70, s96, v151
	ds_read_b64 v[96:97], v71
	ds_read_b64 v[86:87], v70
	v_add_u32_e32 v70, 0x9800, v2
	ds_read2_b32 v[90:91], v70 offset0:64 offset1:96
	v_add_u32_e32 v70, s82, v69
	v_lshlrev_b32_e32 v149, 3, v70
	v_lshl_add_u32 v70, v70, 4, v70
	v_lshlrev_b32_e32 v70, 4, v70
	v_add_u32_e32 v68, 0xd400, v2
	v_add_u32_e32 v145, 0x680, v133
	v_cmp_eq_u32_e32 vcc, 0, v132
	s_waitcnt lgkmcnt(14)
	v_max_f32_e32 v132, v64, v64
	v_max_f32_e32 v165, v130, v130
	v_add_u32_e32 v71, s96, v149
	v_add3_u32 v150, 0, v70, v72
	v_add_u32_e32 v70, s96, v147
	ds_read2_b32 v[78:79], v68 offset0:32 offset1:64
	v_add_u32_e32 v68, s96, v145
	v_add_u32_e32 v73, s76, v69
	v_max_f32_e32 v132, v165, v132
	ds_read_b64 v[84:85], v71
	ds_read_b64 v[80:81], v70
	ds_read_b64 v[70:71], v68
	v_add_u32_e32 v68, 0xdc00, v2
	v_lshlrev_b32_e32 v143, 3, v73
	v_lshl_add_u32 v73, v73, 4, v73
	v_lshlrev_b32_e32 v73, 4, v73
	v_sub_f32_e32 v64, v64, v132
	ds_read2_b32 v[166:167], v2 offset1:32
	ds_read2_b32 v[74:75], v68 offset0:64 offset1:96
	v_add_u32_e32 v68, s96, v143
	v_add3_u32 v144, 0, v73, v72
	v_sub_f32_e32 v130, v130, v132
	v_exp_f32_e32 v64, v64
	ds_read2_b32 v[122:123], v162 offset1:32
	ds_read2_b32 v[116:117], v160 offset1:32
	ds_read2_b32 v[104:105], v156 offset1:32
	ds_read2_b32 v[98:99], v154 offset1:32
	ds_read2_b32 v[88:89], v150 offset1:32
	ds_read2_b32 v[82:83], v148 offset1:32
	ds_read_b64 v[68:69], v68
	ds_read2_b32 v[72:73], v144 offset1:32
	v_exp_f32_e32 v130, v130
	s_waitcnt lgkmcnt(0)
	v_mul_f32_e32 v4, v4, v64
	v_mul_f32_e32 v20, v20, v64
	s_waitcnt lgkmcnt(9)
	v_fmac_f32_e32 v4, v166, v130
	v_fmac_f32_e32 v20, v167, v130
	ds_write2_b32 v2, v4, v20 offset1:32
	s_and_saveexec_b64 s[0:1], vcc
	v_add_u32_e32 v4, 0, v133
	v_mul_f32_e32 v133, v60, v64
	v_add_u32_e32 v4, 0x11000, v4
	v_fmac_f32_e32 v133, v131, v130
	ds_write_b64 v4, v[132:133]
	s_or_b64 exec, exec, s[0:1]
	v_max_f32_e32 v4, v65, v65
	v_max_f32_e32 v20, v126, v126
	v_max_f32_e32 v4, v20, v4
	v_sub_f32_e32 v60, v65, v4
	v_sub_f32_e32 v20, v126, v4
	v_exp_f32_e32 v60, v60
	v_exp_f32_e32 v20, v20
	v_add_u32_e32 v64, 0x880, v2
	v_mul_f32_e32 v5, v5, v60
	v_mul_f32_e32 v21, v21, v60
	v_fmac_f32_e32 v5, v128, v20
	v_fmac_f32_e32 v21, v129, v20
	ds_write2_b32 v64, v5, v21 offset1:32
	s_and_saveexec_b64 s[0:1], vcc
	v_add_u32_e32 v5, 0, v164
	v_add_u32_e32 v21, 0x11000, v5
	v_mul_f32_e32 v5, v61, v60
	v_fmac_f32_e32 v5, v127, v20
	ds_write_b64 v21, v[4:5]
	s_or_b64 exec, exec, s[0:1]
	v_max_f32_e32 v4, v66, v66
	v_max_f32_e32 v5, v120, v120
	v_max_f32_e32 v4, v5, v4
	v_sub_f32_e32 v5, v66, v4
	v_sub_f32_e32 v20, v120, v4
	v_exp_f32_e32 v5, v5
	v_exp_f32_e32 v20, v20
	v_add_u32_e32 v21, 0x1100, v2
	v_mul_f32_e32 v6, v6, v5
	v_mul_f32_e32 v22, v22, v5
	v_fmac_f32_e32 v6, v124, v20
	v_fmac_f32_e32 v22, v125, v20
	ds_write2_b32 v21, v6, v22 offset1:32
	s_and_saveexec_b64 s[0:1], vcc
	v_add_u32_e32 v6, 0, v163
	v_mul_f32_e32 v5, v62, v5
	v_add_u32_e32 v6, 0x11000, v6
	v_fmac_f32_e32 v5, v121, v20
	ds_write_b64 v6, v[4:5]
	s_or_b64 exec, exec, s[0:1]
	v_max_f32_e32 v4, v67, v67
	v_max_f32_e32 v5, v118, v118
	v_max_f32_e32 v4, v5, v4
	v_sub_f32_e32 v5, v67, v4
	v_sub_f32_e32 v6, v118, v4
	v_exp_f32_e32 v5, v5
	v_exp_f32_e32 v6, v6
	v_mul_f32_e32 v7, v7, v5
	v_mul_f32_e32 v20, v23, v5
	s_waitcnt lgkmcnt(10)
; __device__ __forceinline__ int crow(int r, int hi) { return (r & 3) + 8 * (r >> 2) + 4 * hi; }
; template <bool FIRST, int NB> ...
;     ...
; #pragma unroll
;         for (int r = 0; r < 16; ++r) { const int q = crow(r, hi); const int trow = q * trow_mul + trow_add;
;             const float mt = mt4[r >> 2][r & 3], lt = lt4[r >> 2][r & 3], mo = ml[r][0], lo_ = ml[r][1];
;             const float mn = fmaxf(mo, mt); const float fa = __builtin_amdgcn_exp2f(mo - mn), fb = __builtin_amdgcn_exp2f(mt - mn);
;             ACC[trow * ACCP + r32] = a0[r] * fa + o[0][r] * fb; ACC[trow * ACCP + 32 + r32] = a1[r] * fa + o[1][r] * fb;
;             if (r32 == 0) { ML[trow * 2] = mn; ML[trow * 2 + 1] = lo_ * fa + lt * fb; } }
	v_fmac_f32_e32 v7, v122, v6
	v_fmac_f32_e32 v20, v123, v6
	ds_write2_b32 v162, v7, v20 offset1:32
	s_and_saveexec_b64 s[0:1], vcc
	v_add_u32_e32 v7, 0, v161
	v_mul_f32_e32 v5, v63, v5
	v_add_u32_e32 v7, 0x11000, v7
	v_fmac_f32_e32 v5, v119, v6
	ds_write_b64 v7, v[4:5]
	s_or_b64 exec, exec, s[0:1]
	v_max_f32_e32 v4, v56, v56
	v_max_f32_e32 v5, v114, v114
	v_max_f32_e32 v4, v5, v4
	v_sub_f32_e32 v5, v56, v4
	v_sub_f32_e32 v6, v114, v4
	v_exp_f32_e32 v5, v5
	v_exp_f32_e32 v6, v6
	v_mul_f32_e32 v7, v8, v5
	v_mul_f32_e32 v8, v24, v5
	s_waitcnt lgkmcnt(10)
	v_fmac_f32_e32 v7, v116, v6
	v_fmac_f32_e32 v8, v117, v6
	ds_write2_b32 v160, v7, v8 offset1:32
	s_and_saveexec_b64 s[0:1], vcc
	v_add_u32_e32 v7, 0, v159
	v_mul_f32_e32 v5, v52, v5
	v_add_u32_e32 v7, 0x11000, v7
	v_fmac_f32_e32 v5, v115, v6
	ds_write_b64 v7, v[4:5]
	s_or_b64 exec, exec, s[0:1]
	v_max_f32_e32 v4, v57, v57
	v_max_f32_e32 v5, v110, v110
	v_max_f32_e32 v4, v5, v4
	v_sub_f32_e32 v5, v57, v4
	v_sub_f32_e32 v6, v110, v4
	v_exp_f32_e32 v5, v5
	v_exp_f32_e32 v6, v6
	v_add_u32_e32 v7, 0x4c80, v2
	v_mul_f32_e32 v8, v9, v5
	v_mul_f32_e32 v9, v25, v5
	v_fmac_f32_e32 v8, v112, v6
	v_fmac_f32_e32 v9, v113, v6
	ds_write2_b32 v7, v8, v9 offset1:32
	s_and_saveexec_b64 s[0:1], vcc
	v_add_u32_e32 v7, 0, v158
	v_mul_f32_e32 v5, v53, v5
	v_add_u32_e32 v7, 0x11000, v7
	v_fmac_f32_e32 v5, v111, v6
	ds_write_b64 v7, v[4:5]
	s_or_b64 exec, exec, s[0:1]
	v_max_f32_e32 v4, v58, v58
	v_max_f32_e32 v5, v102, v102
	v_max_f32_e32 v4, v5, v4
	v_sub_f32_e32 v5, v58, v4
	v_sub_f32_e32 v6, v102, v4
	v_exp_f32_e32 v5, v5
	v_exp_f32_e32 v6, v6
	v_add_u32_e32 v7, 0x5500, v2
	v_mul_f32_e32 v8, v10, v5
	v_mul_f32_e32 v9, v26, v5
	v_fmac_f32_e32 v8, v106, v6
	v_fmac_f32_e32 v9, v107, v6
	ds_write2_b32 v7, v8, v9 offset1:32
	s_and_saveexec_b64 s[0:1], vcc
	v_add_u32_e32 v7, 0, v157
	v_mul_f32_e32 v5, v54, v5
	v_add_u32_e32 v7, 0x11000, v7
	v_fmac_f32_e32 v5, v103, v6
	ds_write_b64 v7, v[4:5]
	s_or_b64 exec, exec, s[0:1]
	v_max_f32_e32 v4, v59, v59
	v_max_f32_e32 v5, v100, v100
	v_max_f32_e32 v4, v5, v4
	v_sub_f32_e32 v5, v59, v4
	v_sub_f32_e32 v6, v100, v4
	v_exp_f32_e32 v5, v5
	v_exp_f32_e32 v6, v6
	v_mul_f32_e32 v7, v11, v5
	v_mul_f32_e32 v8, v27, v5
	s_waitcnt lgkmcnt(12)
	v_fmac_f32_e32 v7, v104, v6
	v_fmac_f32_e32 v8, v105, v6
	ds_write2_b32 v156, v7, v8 offset1:32
	s_and_saveexec_b64 s[0:1], vcc
	v_add_u32_e32 v7, 0, v155
	v_mul_f32_e32 v5, v55, v5
	v_add_u32_e32 v7, 0x11000, v7
	v_fmac_f32_e32 v5, v101, v6
	ds_write_b64 v7, v[4:5]
	s_or_b64 exec, exec, s[0:1]
	v_max_f32_e32 v4, v48, v48
	v_max_f32_e32 v5, v96, v96
	v_max_f32_e32 v4, v5, v4
	v_sub_f32_e32 v5, v48, v4
	v_sub_f32_e32 v6, v96, v4
	v_exp_f32_e32 v5, v5
	v_exp_f32_e32 v6, v6
	v_mul_f32_e32 v7, v12, v5
	v_mul_f32_e32 v8, v28, v5
	s_waitcnt lgkmcnt(12)
	v_fmac_f32_e32 v7, v98, v6
	v_fmac_f32_e32 v8, v99, v6
	ds_write2_b32 v154, v7, v8 offset1:32
	s_and_saveexec_b64 s[0:1], vcc
	v_add_u32_e32 v7, 0, v153
	v_mul_f32_e32 v5, v44, v5
	v_add_u32_e32 v7, 0x11000, v7
	v_fmac_f32_e32 v5, v97, v6
	ds_write_b64 v7, v[4:5]
	s_or_b64 exec, exec, s[0:1]
	v_max_f32_e32 v4, v49, v49
	v_max_f32_e32 v5, v92, v92
	v_max_f32_e32 v4, v5, v4
	v_sub_f32_e32 v5, v49, v4
	v_sub_f32_e32 v6, v92, v4
	v_exp_f32_e32 v5, v5
	v_exp_f32_e32 v6, v6
	v_add_u32_e32 v7, 0x9080, v2
	v_mul_f32_e32 v8, v13, v5
	v_mul_f32_e32 v9, v29, v5
	v_fmac_f32_e32 v8, v94, v6
	v_fmac_f32_e32 v9, v95, v6
	ds_write2_b32 v7, v8, v9 offset1:32
	s_and_saveexec_b64 s[0:1], vcc
	v_add_u32_e32 v7, 0, v152
	v_mul_f32_e32 v5, v45, v5
	v_add_u32_e32 v7, 0x11000, v7
	v_fmac_f32_e32 v5, v93, v6
	ds_write_b64 v7, v[4:5]
	s_or_b64 exec, exec, s[0:1]
	v_max_f32_e32 v4, v50, v50
	v_max_f32_e32 v5, v86, v86
	v_max_f32_e32 v4, v5, v4
	v_sub_f32_e32 v5, v50, v4
	v_sub_f32_e32 v6, v86, v4
	v_exp_f32_e32 v5, v5
	v_exp_f32_e32 v6, v6
	v_add_u32_e32 v7, 0x9900, v2
	v_mul_f32_e32 v8, v14, v5
	v_mul_f32_e32 v9, v30, v5
	v_fmac_f32_e32 v8, v90, v6
	v_fmac_f32_e32 v9, v91, v6
	ds_write2_b32 v7, v8, v9 offset1:32
	s_and_saveexec_b64 s[0:1], vcc
	v_add_u32_e32 v7, 0, v151
	v_mul_f32_e32 v5, v46, v5
	v_add_u32_e32 v7, 0x11000, v7
	v_fmac_f32_e32 v5, v87, v6
	ds_write_b64 v7, v[4:5]
	s_or_b64 exec, exec, s[0:1]
	v_max_f32_e32 v4, v51, v51
	v_max_f32_e32 v5, v84, v84
	v_max_f32_e32 v4, v5, v4
	v_sub_f32_e32 v5, v51, v4
	v_sub_f32_e32 v6, v84, v4
	v_exp_f32_e32 v5, v5
	v_exp_f32_e32 v6, v6
	v_mul_f32_e32 v7, v15, v5
	v_mul_f32_e32 v8, v31, v5
	s_waitcnt lgkmcnt(14)
	v_fmac_f32_e32 v7, v88, v6
	v_fmac_f32_e32 v8, v89, v6
	ds_write2_b32 v150, v7, v8 offset1:32
	s_and_saveexec_b64 s[0:1], vcc
	v_add_u32_e32 v7, 0, v149
	v_mul_f32_e32 v5, v47, v5
	v_add_u32_e32 v7, 0x11000, v7
	v_fmac_f32_e32 v5, v85, v6
	ds_write_b64 v7, v[4:5]
	s_or_b64 exec, exec, s[0:1]
	v_max_f32_e32 v4, v40, v40
	v_max_f32_e32 v5, v80, v80
	v_max_f32_e32 v4, v5, v4
	v_sub_f32_e32 v5, v40, v4
	v_sub_f32_e32 v6, v80, v4
	v_exp_f32_e32 v5, v5
	v_exp_f32_e32 v6, v6
	v_mul_f32_e32 v7, v16, v5
	v_mul_f32_e32 v8, v32, v5
	s_waitcnt lgkmcnt(14)
	v_fmac_f32_e32 v7, v82, v6
	v_fmac_f32_e32 v8, v83, v6
	ds_write2_b32 v148, v7, v8 offset1:32
	s_and_saveexec_b64 s[0:1], vcc
	v_add_u32_e32 v7, 0, v147
	v_mul_f32_e32 v5, v36, v5
	v_add_u32_e32 v7, 0x11000, v7
	v_fmac_f32_e32 v5, v81, v6
	ds_write_b64 v7, v[4:5]
	s_or_b64 exec, exec, s[0:1]
	v_max_f32_e32 v4, v41, v41
	v_max_f32_e32 v5, v76, v76
	v_max_f32_e32 v4, v5, v4
	v_sub_f32_e32 v5, v41, v4
	v_sub_f32_e32 v6, v76, v4
	v_exp_f32_e32 v5, v5
	v_exp_f32_e32 v6, v6
	v_add_u32_e32 v7, 0xd480, v2
	v_mul_f32_e32 v8, v17, v5
	v_mul_f32_e32 v9, v33, v5
	v_fmac_f32_e32 v8, v78, v6
	v_fmac_f32_e32 v9, v79, v6
	ds_write2_b32 v7, v8, v9 offset1:32
	s_and_saveexec_b64 s[0:1], vcc
	v_add_u32_e32 v7, 0, v146
	v_mul_f32_e32 v5, v37, v5
	v_add_u32_e32 v7, 0x11000, v7
	v_fmac_f32_e32 v5, v77, v6
	ds_write_b64 v7, v[4:5]
	s_or_b64 exec, exec, s[0:1]
	v_max_f32_e32 v4, v42, v42
	v_max_f32_e32 v5, v70, v70
	v_max_f32_e32 v4, v5, v4
	v_sub_f32_e32 v5, v42, v4
	v_sub_f32_e32 v6, v70, v4
	v_exp_f32_e32 v5, v5
	v_exp_f32_e32 v6, v6
	v_add_u32_e32 v2, 0xdd00, v2
	v_mul_f32_e32 v7, v18, v5
	v_mul_f32_e32 v8, v34, v5
	v_fmac_f32_e32 v7, v74, v6
	v_fmac_f32_e32 v8, v75, v6
	ds_write2_b32 v2, v7, v8 offset1:32
	s_and_saveexec_b64 s[0:1], vcc
	v_add_u32_e32 v2, 0, v145
	v_mul_f32_e32 v5, v38, v5
	v_add_u32_e32 v2, 0x11000, v2
	v_fmac_f32_e32 v5, v71, v6
	ds_write_b64 v2, v[4:5]
	s_or_b64 exec, exec, s[0:1]
	v_max_f32_e32 v2, v43, v43
	s_waitcnt lgkmcnt(14)
	v_max_f32_e32 v4, v68, v68
	v_max_f32_e32 v4, v4, v2
	v_sub_f32_e32 v5, v43, v4
	v_sub_f32_e32 v2, v68, v4
	v_exp_f32_e32 v5, v5
	v_exp_f32_e32 v2, v2
	v_mul_f32_e32 v6, v19, v5
	v_mul_f32_e32 v7, v35, v5
	v_fmac_f32_e32 v6, v72, v2
	v_fmac_f32_e32 v7, v73, v2
	ds_write2_b32 v144, v6, v7 offset1:32
	s_and_saveexec_b64 s[0:1], vcc
	s_cbranch_execz .LBB0_301
	v_add_u32_e32 v6, 0, v143
	v_mul_f32_e32 v5, v39, v5
	v_add_u32_e32 v6, 0x11000, v6
	v_fmac_f32_e32 v5, v69, v2
	ds_write_b64 v6, v[4:5]
	s_branch .LBB0_301
